# GEMM3 epilogue: residual loads software-pipelined one row group ahead (no stores in the load waits)
# speedup vs baseline: 1.0144x; 1.0144x over previous
; __device__ __forceinline__ unsigned cvt_pk_bf16(float lo, float hi) { unsigned r; asm volatile("v_cvt_pk_bf16_f32 %0, %1, %2" : "=v"(r) : "v"(lo), "v"(hi)); return r; }
;     __device__ __forceinline__ void operator()(const f32x4 (&acc)[2][2][4][2], const Unit& u, int wr, int wc, int fr, int fq) const {
;     ...
;         f32x4 gv[2][2];
; #pragma unroll
;         for (int bj = 0; bj < 2; ++bj)
; #pragma unroll
;             for (int n = 0; n < 2; ++n) gv[bj][n] = *(const f32x4*)(gain + col0 + bj * HALF + 4 * n);
;         float* SSQP = (float*)(ws + OFF_SSQP); unsigned char* Q8 = ws + OFF_Q8;
; #pragma unroll
;         for (int ai = 0; ai < 2; ++ai)
; #pragma unroll
;             for (int m = 0; m < 4; ++m) { const size_t r = (size_t)(row0 + ai * HALF + m * 16); float ss = 0.f;
; #pragma unroll
;                 for (int bj = 0; bj < 2; ++bj) { const size_t off = r * 4096 + col0 + bj * HALF;
;                     const f32x4 v0 = acc[ai][bj][m][0] * scale + *(const f32x4*)(R + off), v1 = acc[ai][bj][m][1] * scale + *(const f32x4*)(R + off + 4);
;                     ss += (v0[0] * v0[0] + v0[1] * v0[1]) + (v0[2] * v0[2] + v0[3] * v0[3]) + (v1[0] * v1[0] + v1[1] * v1[1]) + (v1[2] * v1[2] + v1[3] * v1[3]);
;                     u32x4 w; w.x = cvt_pk_bf16(v0[0], v0[1]); w.y = cvt_pk_bf16(v0[2], v0[3]); w.z = cvt_pk_bf16(v1[0], v1[1]); w.w = cvt_pk_bf16(v1[2], v1[3]);
;                     *(u32x4*)(HB + off) = w;
;                     u32x2e q; q.x = q8x4(v0, gv[bj][0], (float)HQS); q.y = q8x4(v1, gv[bj][1], (float)HQS);
;                     *(u32x2e*)(Q8 + r * LDQ8 + col0 + bj * HALF) = q; }
.LBB0_617:
	v_lshl_add_u32 v140, s29, 8, v169
	v_lshl_or_b32 v138, s28, 8, v170
	v_ashrrev_i32_e32 v141, 31, v140
	v_ashrrev_i32_e32 v139, 31, v138
	v_lshlrev_b64 v[66:67], 12, v[140:141]
	v_lshl_add_u64 v[154:155], v[66:67], 0, v[138:139]
	v_lshl_add_u64 v[156:157], v[154:155], 2, s[8:9]
	global_load_dwordx4 v[146:149], v[156:157], off
	global_load_dwordx4 v[150:153], v[156:157], off offset:16
	v_lshlrev_b32_e32 v252, 2, v154
	global_load_dwordx4 v[244:247], v252, s[8:9] offset:512
	global_load_dwordx4 v[248:251], v252, s[8:9] offset:528
	v_lshl_add_u64 v[144:145], v[138:139], 2, s[52:53]
	global_load_dwordx4 v[74:77], v[144:145], off
	global_load_dwordx4 v[66:69], v[144:145], off offset:16
	v_cvt_f32_i32_e32 v159, v63
	v_cvt_f32_i32_e32 v158, v62
	v_cvt_f32_i32_e32 v161, v65
	v_cvt_f32_i32_e32 v160, v64
	v_cvt_f32_i32_e32 v179, v51
	v_cvt_f32_i32_e32 v178, v50
	v_cvt_f32_i32_e32 v181, v53
	v_cvt_f32_i32_e32 v180, v52
	v_lshlrev_b64 v[154:155], 1, v[154:155]
	global_load_dwordx4 v[50:53], v[144:145], off offset:528
	global_load_dwordx4 v[62:65], v[144:145], off offset:512
	s_add_u32 s98, s8, 0x40000
	s_addc_u32 s99, s9, 0
	global_load_dwordx4 v[212:215], v252, s[98:99]
	global_load_dwordx4 v[216:219], v252, s[98:99] offset:16
	global_load_dwordx4 v[220:223], v252, s[98:99] offset:512
	global_load_dwordx4 v[224:227], v252, s[98:99] offset:528
	v_lshl_add_u64 v[182:183], s[14:15], 0, v[154:155]
	v_readlane_b32 s22, v255, 13
	v_readlane_b32 s23, v255, 14
	v_cvt_f32_i32_e32 v135, v135
	v_cvt_f32_i32_e32 v134, v134
	v_lshl_add_u64 v[142:143], s[22:23], 0, v[138:139]
	v_mad_i64_i32 v[144:145], s[22:23], v140, s50, v[142:143]
	v_cvt_f32_i32_e32 v137, v137
	v_cvt_f32_i32_e32 v136, v136
	v_cvt_f32_i32_e32 v131, v131
	v_cvt_f32_i32_e32 v130, v130
	v_or_b32_e32 v154, 0x100, v154
	v_lshl_add_u64 v[154:155], s[14:15], 0, v[154:155]
	s_lshl_b32 s22, s28, 2
	s_ashr_i32 s23, s22, 31
	s_lshl_b64 s[22:23], s[22:23], 2
	s_add_u32 s22, s48, s22
	s_addc_u32 s23, s49, s23
	s_waitcnt vmcnt(11)
	v_pk_fma_f32 v[160:161], v[160:161], s[26:27], v[148:149] op_sel_hi:[1,0,1]
	v_pk_fma_f32 v[158:159], v[158:159], s[26:27], v[146:147] op_sel_hi:[1,0,1]
	s_waitcnt vmcnt(10)
	v_pk_fma_f32 v[180:181], v[180:181], s[26:27], v[152:153] op_sel_hi:[1,0,1]
	v_pk_fma_f32 v[178:179], v[178:179], s[26:27], v[150:151] op_sel_hi:[1,0,1]
	v_cvt_pk_bf16_f32 v146, v158, v159
	v_cvt_pk_bf16_f32 v147, v160, v161
	s_waitcnt vmcnt(7)
	v_mul_f32_e32 v150, v74, v158
	v_cvt_pk_bf16_f32 v148, v178, v179
	v_cvt_pk_bf16_f32 v149, v180, v181
	v_mul_f32_e32 v151, v75, v159
	v_mul_f32_e32 v152, v76, v160
	v_mul_f32_e32 v153, v77, v161
	s_waitcnt vmcnt(6)
	v_mul_f32_e32 v184, v66, v178
	v_mul_f32_e32 v185, v67, v179
	v_mul_f32_e32 v186, v68, v180
	v_mul_f32_e32 v187, v69, v181
	global_store_dwordx4 v[182:183], v[146:149], off
	v_mul_f32_e32 v159, v159, v159
	v_mul_f32_e32 v161, v161, v161
	v_mul_f32_e32 v146, 0x41c00000, v150
	v_mul_f32_e32 v147, 0x41c00000, v151
	v_mul_f32_e32 v148, 0x41c00000, v152
	v_mul_f32_e32 v149, 0x41c00000, v153
	v_mul_f32_e32 v150, 0x41c00000, v184
	v_mul_f32_e32 v151, 0x41c00000, v185
	v_mul_f32_e32 v152, 0x41c00000, v186
	v_mul_f32_e32 v153, 0x41c00000, v187
	v_med3_f32 v146, v146, s51, v177
	v_med3_f32 v147, v147, s51, v177
	v_med3_f32 v148, v148, s51, v177
	v_med3_f32 v149, v149, s51, v177
	v_med3_f32 v150, v150, s51, v177
	v_med3_f32 v151, v151, s51, v177
	v_med3_f32 v152, v152, s51, v177
	v_med3_f32 v153, v153, s51, v177
	v_add_f32_e32 v146, 0x4b400000, v146
	v_add_f32_e32 v147, 0x4b400000, v147
	v_add_f32_e32 v148, 0x4b400000, v148
	v_add_f32_e32 v149, 0x4b400000, v149
	v_add_f32_e32 v150, 0x4b400000, v150
	v_add_f32_e32 v151, 0x4b400000, v151
	v_add_f32_e32 v152, 0x4b400000, v152
	v_add_f32_e32 v153, 0x4b400000, v153
	v_perm_b32 v146, v147, v146, s56
	v_perm_b32 v147, v149, v148, s57
	v_perm_b32 v148, v151, v150, s56
	v_perm_b32 v149, v153, v152, s57
	v_or_b32_e32 v146, v146, v147
	v_or_b32_e32 v147, v148, v149
	global_store_dwordx2 v[144:145], v[146:147], off
	s_nop 0
	s_nop 0
	s_nop 0
	v_cvt_f32_i32_e32 v157, v133
	v_cvt_f32_i32_e32 v156, v132
	v_and_b32_e32 v133, 64, v176
	v_mul_f32_e32 v179, v179, v179
	v_fmac_f32_e32 v159, v158, v158
	v_fmac_f32_e32 v161, v160, v160
	v_xor_b32_e32 v132, 16, v176
	v_add_u32_e32 v133, 64, v133
	v_mul_f32_e32 v181, v181, v181
	v_fmac_f32_e32 v179, v178, v178
	v_add_f32_e32 v158, v159, v161
	v_cmp_lt_i32_e32 vcc, v132, v133
	v_fmac_f32_e32 v181, v180, v180
	v_add_f32_e32 v158, v158, v179
	v_cndmask_b32_e32 v132, v176, v132, vcc
	v_add_f32_e32 v158, v181, v158
	v_lshlrev_b32_e32 v132, 2, v132
	v_xor_b32_e32 v182, 32, v176
	v_cmp_lt_i32_e32 vcc, v182, v133
	s_waitcnt vmcnt(6)
	v_pk_fma_f32 v[148:149], v[136:137], s[26:27], v[246:247] op_sel_hi:[1,0,1]
	v_pk_fma_f32 v[146:147], v[134:135], s[26:27], v[244:245] op_sel_hi:[1,0,1]
	s_waitcnt vmcnt(6)
; __device__ __forceinline__ unsigned cvt_pk_bf16(float lo, float hi) { unsigned r; asm volatile("v_cvt_pk_bf16_f32 %0, %1, %2" : "=v"(r) : "v"(lo), "v"(hi)); return r; }
;     __device__ __forceinline__ void operator()(const f32x4 (&acc)[2][2][4][2], const Unit& u, int wr, int wc, int fr, int fq) const {
;     ...
;             for (int m = 0; m < 4; ++m) { const size_t r = (size_t)(row0 + ai * HALF + m * 16); float ss = 0.f;
; #pragma unroll
;                 for (int bj = 0; bj < 2; ++bj) { const size_t off = r * 4096 + col0 + bj * HALF;
;                     const f32x4 v0 = acc[ai][bj][m][0] * scale + *(const f32x4*)(R + off), v1 = acc[ai][bj][m][1] * scale + *(const f32x4*)(R + off + 4);
;                     ss += (v0[0] * v0[0] + v0[1] * v0[1]) + (v0[2] * v0[2] + v0[3] * v0[3]) + (v1[0] * v1[0] + v1[1] * v1[1]) + (v1[2] * v1[2] + v1[3] * v1[3]);
;                     u32x4 w; w.x = cvt_pk_bf16(v0[0], v0[1]); w.y = cvt_pk_bf16(v0[2], v0[3]); w.z = cvt_pk_bf16(v1[0], v1[1]); w.w = cvt_pk_bf16(v1[2], v1[3]);
;                     *(u32x4*)(HB + off) = w;
;                     u32x2e q; q.x = q8x4(v0, gv[bj][0], (float)HQS); q.y = q8x4(v1, gv[bj][1], (float)HQS);
;                     *(u32x2e*)(Q8 + r * LDQ8 + col0 + bj * HALF) = q; }
;                 ss += __shfl_xor(ss, 16); ss += __shfl_xor(ss, 32);
;                 if (fq == 0) SSQP[r * 64 + u.pn * 4 + wc] = ss; }
	v_pk_fma_f32 v[130:131], v[130:131], s[26:27], v[248:249] op_sel_hi:[1,0,1]
	v_mul_f32_e32 v150, v147, v147
	v_mul_f32_e32 v151, v149, v149
	v_pk_fma_f32 v[152:153], v[156:157], s[26:27], v[250:251] op_sel_hi:[1,0,1]
	v_mul_f32_e32 v156, v131, v131
	v_cvt_pk_bf16_f32 v134, v146, v147
	v_cvt_pk_bf16_f32 v135, v148, v149
	v_cvt_pk_bf16_f32 v136, v130, v131
	v_mul_f32_e32 v131, v51, v131
	v_fmac_f32_e32 v150, v146, v146
	v_fmac_f32_e32 v151, v148, v148
	v_mul_f32_e32 v157, v153, v153
	v_mul_f32_e32 v160, v64, v148
	v_fmac_f32_e32 v156, v130, v130
	v_mul_f32_e32 v131, 0x41c00000, v131
	v_add_f32_e32 v148, v150, v151
	v_mul_f32_e32 v149, v65, v149
	v_fmac_f32_e32 v157, v152, v152
	v_med3_f32 v131, v131, s51, v177
	v_add_f32_e32 v148, v148, v156
	v_cvt_pk_bf16_f32 v137, v152, v153
	global_store_dwordx4 v[154:155], v[134:137], off
	v_mul_f32_e32 v159, v62, v146
	v_mul_f32_e32 v147, v63, v147
	v_mul_f32_e32 v136, 0x41c00000, v149
	v_add_f32_e32 v149, 0x4b400000, v131
	v_add_f32_e32 v131, v157, v148
	v_add_f32_e32 v131, v158, v131
	ds_bpermute_b32 v148, v132, v131
	v_mul_f32_e32 v161, v50, v130
	v_mul_f32_e32 v130, 0x41c00000, v159
	v_mul_f32_e32 v134, 0x41c00000, v147
	v_mul_f32_e32 v135, 0x41c00000, v160
	v_med3_f32 v130, v130, s51, v177
	v_med3_f32 v134, v134, s51, v177
	v_med3_f32 v135, v135, s51, v177
	v_med3_f32 v136, v136, s51, v177
	v_add_f32_e32 v130, 0x4b400000, v130
	v_add_f32_e32 v134, 0x4b400000, v134
	v_add_f32_e32 v135, 0x4b400000, v135
	v_add_f32_e32 v136, 0x4b400000, v136
	v_cndmask_b32_e32 v133, v176, v182, vcc
	v_perm_b32 v130, v134, v130, s56
	v_perm_b32 v134, v136, v135, s57
	v_mul_f32_e32 v178, v52, v152
	v_mul_f32_e32 v153, v53, v153
	v_or_b32_e32 v134, v130, v134
	s_waitcnt lgkmcnt(0)
	v_add_f32_e32 v130, v131, v148
	v_lshlrev_b32_e32 v133, 2, v133
	v_mul_f32_e32 v137, 0x41c00000, v161
	v_mul_f32_e32 v146, 0x41c00000, v178
	v_mul_f32_e32 v147, 0x41c00000, v153
	ds_bpermute_b32 v131, v133, v130
	v_med3_f32 v137, v137, s51, v177
	v_med3_f32 v146, v146, s51, v177
	v_med3_f32 v147, v147, s51, v177
	v_add_f32_e32 v137, 0x4b400000, v137
	v_add_f32_e32 v146, 0x4b400000, v146
	v_add_f32_e32 v147, 0x4b400000, v147
	v_perm_b32 v135, v149, v137, s56
	v_perm_b32 v136, v147, v146, s57
	v_or_b32_e32 v135, v135, v136
	global_store_dwordx2 v[144:145], v[134:135], off offset:128
	s_and_saveexec_b64 s[28:29], s[0:1]
	s_cbranch_execz .LBB0_619
	v_lshlrev_b64 v[134:135], 8, v[140:141]
	v_lshl_add_u64 v[134:135], s[22:23], 0, v[134:135]
	s_waitcnt lgkmcnt(0)
	v_add_f32_e32 v130, v130, v131
	global_store_dword v[134:135], v130, off
.LBB0_619:
	s_or_b64 exec, exec, s[28:29]
	s_add_u32 s98, s8, 0x80000
	s_addc_u32 s99, s9, 0
	global_load_dwordx4 v[228:231], v252, s[98:99]
	global_load_dwordx4 v[232:235], v252, s[98:99] offset:16
	global_load_dwordx4 v[236:239], v252, s[98:99] offset:512
	global_load_dwordx4 v[240:243], v252, s[98:99] offset:528
	v_or_b32_e32 v130, 16, v140
	s_waitcnt lgkmcnt(0)
	v_ashrrev_i32_e32 v131, 31, v130
	v_lshlrev_b64 v[134:135], 12, v[130:131]
	v_lshl_add_u64 v[148:149], v[134:135], 0, v[138:139]
	v_lshl_add_u64 v[150:151], v[148:149], 2, s[8:9]
	s_nop 0
	s_nop 0
	v_cvt_f32_i32_e32 v127, v127
	v_cvt_f32_i32_e32 v126, v126
	v_cvt_f32_i32_e32 v129, v129
	v_cvt_f32_i32_e32 v128, v128
	v_cvt_f32_i32_e32 v153, v123
	v_cvt_f32_i32_e32 v152, v122
	v_cvt_f32_i32_e32 v125, v125
	v_cvt_f32_i32_e32 v124, v124
	v_lshlrev_b64 v[148:149], 1, v[148:149]
	v_lshl_add_u64 v[154:155], s[14:15], 0, v[148:149]
	v_mad_i64_i32 v[122:123], s[28:29], v130, s50, v[142:143]
	v_cvt_f32_i32_e32 v119, v119
	v_cvt_f32_i32_e32 v118, v118
	v_cvt_f32_i32_e32 v121, v121
	v_cvt_f32_i32_e32 v120, v120
	v_cvt_f32_i32_e32 v115, v115
	v_cvt_f32_i32_e32 v114, v114
	v_cvt_f32_i32_e32 v117, v117
	v_cvt_f32_i32_e32 v116, v116
	v_or_b32_e32 v148, 0x100, v148
	v_lshl_add_u64 v[148:149], s[14:15], 0, v[148:149]
	s_waitcnt vmcnt(8)
	v_pk_fma_f32 v[128:129], v[128:129], s[26:27], v[214:215] op_sel_hi:[1,0,1]
	v_pk_fma_f32 v[156:157], v[126:127], s[26:27], v[212:213] op_sel_hi:[1,0,1]
	s_waitcnt vmcnt(8)
	v_pk_fma_f32 v[146:147], v[124:125], s[26:27], v[218:219] op_sel_hi:[1,0,1]
	v_pk_fma_f32 v[144:145], v[152:153], s[26:27], v[216:217] op_sel_hi:[1,0,1]
	v_cvt_pk_bf16_f32 v124, v156, v157
	v_cvt_pk_bf16_f32 v125, v128, v129
	v_mul_f32_e32 v134, v74, v156
	v_cvt_pk_bf16_f32 v126, v144, v145
	v_cvt_pk_bf16_f32 v127, v146, v147
	v_mul_f32_e32 v135, v75, v157
	v_mul_f32_e32 v136, v76, v128
	v_mul_f32_e32 v137, v77, v129
	v_mul_f32_e32 v141, v66, v144
	v_mul_f32_e32 v152, v67, v145
	v_mul_f32_e32 v153, v68, v146
	v_mul_f32_e32 v158, v69, v147
	global_store_dwordx4 v[154:155], v[124:127], off
	v_mul_f32_e32 v129, v129, v129
	v_fmac_f32_e32 v129, v128, v128
	v_mul_f32_e32 v124, 0x41c00000, v134
	v_mul_f32_e32 v125, 0x41c00000, v135
	v_mul_f32_e32 v126, 0x41c00000, v136
	v_mul_f32_e32 v127, 0x41c00000, v137
	v_mul_f32_e32 v134, 0x41c00000, v141
	v_mul_f32_e32 v135, 0x41c00000, v152
	v_mul_f32_e32 v136, 0x41c00000, v153
	v_mul_f32_e32 v137, 0x41c00000, v158
	v_med3_f32 v124, v124, s51, v177
	v_med3_f32 v125, v125, s51, v177
	v_med3_f32 v126, v126, s51, v177
	v_med3_f32 v127, v127, s51, v177
	v_med3_f32 v134, v134, s51, v177
	v_med3_f32 v135, v135, s51, v177
	v_med3_f32 v136, v136, s51, v177
	v_med3_f32 v137, v137, s51, v177
	v_add_f32_e32 v124, 0x4b400000, v124
	v_add_f32_e32 v125, 0x4b400000, v125
	v_add_f32_e32 v126, 0x4b400000, v126
	v_add_f32_e32 v127, 0x4b400000, v127
	v_add_f32_e32 v134, 0x4b400000, v134
	v_add_f32_e32 v135, 0x4b400000, v135
	v_add_f32_e32 v136, 0x4b400000, v136
	v_add_f32_e32 v137, 0x4b400000, v137
	v_perm_b32 v124, v125, v124, s56
	v_perm_b32 v125, v127, v126, s57
	v_perm_b32 v126, v135, v134, s56
	v_perm_b32 v127, v137, v136, s57
	v_or_b32_e32 v124, v124, v125
	v_or_b32_e32 v125, v126, v127
	global_store_dwordx2 v[122:123], v[124:125], off
	s_nop 0
	s_nop 0
	s_nop 0
	v_mul_f32_e32 v141, v157, v157
	v_fmac_f32_e32 v141, v156, v156
	v_add_f32_e32 v128, v141, v129
	v_mul_f32_e32 v145, v145, v145
	v_mul_f32_e32 v147, v147, v147
	v_fmac_f32_e32 v145, v144, v144
	v_fmac_f32_e32 v147, v146, v146
	v_add_f32_e32 v128, v128, v145
	v_add_f32_e32 v128, v147, v128
	s_waitcnt vmcnt(11)
; __device__ __forceinline__ unsigned cvt_pk_bf16(float lo, float hi) { unsigned r; asm volatile("v_cvt_pk_bf16_f32 %0, %1, %2" : "=v"(r) : "v"(lo), "v"(hi)); return r; }
;     __device__ __forceinline__ void operator()(const f32x4 (&acc)[2][2][4][2], const Unit& u, int wr, int wc, int fr, int fq) const {
;     ...
;             for (int m = 0; m < 4; ++m) { const size_t r = (size_t)(row0 + ai * HALF + m * 16); float ss = 0.f;
; #pragma unroll
;                 for (int bj = 0; bj < 2; ++bj) { const size_t off = r * 4096 + col0 + bj * HALF;
;                     const f32x4 v0 = acc[ai][bj][m][0] * scale + *(const f32x4*)(R + off), v1 = acc[ai][bj][m][1] * scale + *(const f32x4*)(R + off + 4);
;                     ss += (v0[0] * v0[0] + v0[1] * v0[1]) + (v0[2] * v0[2] + v0[3] * v0[3]) + (v1[0] * v1[0] + v1[1] * v1[1]) + (v1[2] * v1[2] + v1[3] * v1[3]);
;                     u32x4 w; w.x = cvt_pk_bf16(v0[0], v0[1]); w.y = cvt_pk_bf16(v0[2], v0[3]); w.z = cvt_pk_bf16(v1[0], v1[1]); w.w = cvt_pk_bf16(v1[2], v1[3]);
;                     *(u32x4*)(HB + off) = w;
;                     u32x2e q; q.x = q8x4(v0, gv[bj][0], (float)HQS); q.y = q8x4(v1, gv[bj][1], (float)HQS);
;                     *(u32x2e*)(Q8 + r * LDQ8 + col0 + bj * HALF) = q; }
;                 ss += __shfl_xor(ss, 16); ss += __shfl_xor(ss, 32);
;                 if (fq == 0) SSQP[r * 64 + u.pn * 4 + wc] = ss; }
	v_pk_fma_f32 v[120:121], v[120:121], s[26:27], v[222:223] op_sel_hi:[1,0,1]
	v_pk_fma_f32 v[118:119], v[118:119], s[26:27], v[220:221] op_sel_hi:[1,0,1]
	s_waitcnt vmcnt(11)
	v_pk_fma_f32 v[126:127], v[114:115], s[26:27], v[224:225] op_sel_hi:[1,0,1]
	v_mul_f32_e32 v129, v119, v119
	v_mul_f32_e32 v134, v121, v121
	v_pk_fma_f32 v[124:125], v[116:117], s[26:27], v[226:227] op_sel_hi:[1,0,1]
	v_mul_f32_e32 v135, v127, v127
	v_cvt_pk_bf16_f32 v114, v118, v119
	v_cvt_pk_bf16_f32 v115, v120, v121
	v_cvt_pk_bf16_f32 v116, v126, v127
	v_cvt_pk_bf16_f32 v117, v124, v125
	v_mul_f32_e32 v137, v62, v118
	v_mul_f32_e32 v119, v63, v119
	v_mul_f32_e32 v141, v64, v120
	v_mul_f32_e32 v121, v65, v121
	v_fmac_f32_e32 v129, v118, v118
	v_fmac_f32_e32 v134, v120, v120
	v_mul_f32_e32 v136, v125, v125
	v_fmac_f32_e32 v135, v126, v126
	global_store_dwordx4 v[148:149], v[114:117], off
	v_fmac_f32_e32 v136, v124, v124
	v_mul_f32_e32 v144, v50, v126
	v_mul_f32_e32 v114, 0x41c00000, v137
	v_mul_f32_e32 v115, 0x41c00000, v119
	v_mul_f32_e32 v116, 0x41c00000, v141
	v_mul_f32_e32 v117, 0x41c00000, v121
	v_add_f32_e32 v121, v129, v134
	v_med3_f32 v114, v114, s51, v177
	v_med3_f32 v115, v115, s51, v177
	v_med3_f32 v116, v116, s51, v177
	v_med3_f32 v117, v117, s51, v177
	v_add_f32_e32 v121, v121, v135
	v_add_f32_e32 v114, 0x4b400000, v114
	v_add_f32_e32 v115, 0x4b400000, v115
	v_add_f32_e32 v116, 0x4b400000, v116
	v_add_f32_e32 v117, 0x4b400000, v117
	v_add_f32_e32 v121, v136, v121
	v_perm_b32 v114, v115, v114, s56
	v_perm_b32 v115, v117, v116, s57
	v_add_f32_e32 v117, v128, v121
	v_or_b32_e32 v116, v114, v115
	ds_bpermute_b32 v114, v132, v117
	v_mul_f32_e32 v115, v53, v125
	v_mul_f32_e32 v115, 0x41c00000, v115
	v_mul_f32_e32 v127, v51, v127
	v_mul_f32_e32 v145, v52, v124
	v_med3_f32 v115, v115, s51, v177
	s_waitcnt lgkmcnt(0)
	v_add_f32_e32 v114, v117, v114
	v_mul_f32_e32 v118, 0x41c00000, v144
	v_mul_f32_e32 v119, 0x41c00000, v127
	v_mul_f32_e32 v120, 0x41c00000, v145
	v_add_f32_e32 v121, 0x4b400000, v115
	ds_bpermute_b32 v115, v133, v114
	v_med3_f32 v118, v118, s51, v177
	v_med3_f32 v119, v119, s51, v177
	v_med3_f32 v120, v120, s51, v177
	v_add_f32_e32 v118, 0x4b400000, v118
	v_add_f32_e32 v119, 0x4b400000, v119
	v_add_f32_e32 v120, 0x4b400000, v120
	v_perm_b32 v117, v119, v118, s56
	v_perm_b32 v118, v121, v120, s57
	v_or_b32_e32 v117, v117, v118
	global_store_dwordx2 v[122:123], v[116:117], off offset:128
	s_and_saveexec_b64 s[28:29], s[0:1]
	s_cbranch_execz .LBB0_621
	v_lshlrev_b64 v[116:117], 8, v[130:131]
	v_lshl_add_u64 v[116:117], s[22:23], 0, v[116:117]
	s_waitcnt lgkmcnt(0)
	v_add_f32_e32 v114, v114, v115
	global_store_dword v[116:117], v114, off
.LBB0_621:
	s_or_b64 exec, exec, s[28:29]
	s_add_u32 s98, s8, 0xc0000
	s_addc_u32 s99, s9, 0
	global_load_dwordx4 v[212:215], v252, s[98:99]
	global_load_dwordx4 v[216:219], v252, s[98:99] offset:16
	global_load_dwordx4 v[220:223], v252, s[98:99] offset:512
	global_load_dwordx4 v[224:227], v252, s[98:99] offset:528
	v_or_b32_e32 v114, 32, v140
	s_waitcnt lgkmcnt(0)
	v_ashrrev_i32_e32 v115, 31, v114
	v_lshlrev_b64 v[116:117], 12, v[114:115]
	v_lshl_add_u64 v[124:125], v[116:117], 0, v[138:139]
	v_lshl_add_u64 v[126:127], v[124:125], 2, s[8:9]
	s_nop 0
	s_nop 0
	v_cvt_f32_i32_e32 v111, v111
	v_cvt_f32_i32_e32 v110, v110
	v_cvt_f32_i32_e32 v113, v113
	v_cvt_f32_i32_e32 v112, v112
	v_cvt_f32_i32_e32 v129, v107
	v_cvt_f32_i32_e32 v128, v106
	v_cvt_f32_i32_e32 v109, v109
	v_cvt_f32_i32_e32 v108, v108
	v_lshlrev_b64 v[124:125], 1, v[124:125]
	v_lshl_add_u64 v[130:131], s[14:15], 0, v[124:125]
	v_mad_i64_i32 v[106:107], s[28:29], v114, s50, v[142:143]
	v_cvt_f32_i32_e32 v103, v103
	v_cvt_f32_i32_e32 v102, v102
	v_cvt_f32_i32_e32 v105, v105
	v_cvt_f32_i32_e32 v104, v104
	v_cvt_f32_i32_e32 v99, v99
	v_cvt_f32_i32_e32 v98, v98
	v_cvt_f32_i32_e32 v101, v101
	v_cvt_f32_i32_e32 v100, v100
	v_or_b32_e32 v124, 0x100, v124
	v_lshl_add_u64 v[124:125], s[14:15], 0, v[124:125]
	s_waitcnt vmcnt(8)
	v_pk_fma_f32 v[112:113], v[112:113], s[26:27], v[230:231] op_sel_hi:[1,0,1]
	v_pk_fma_f32 v[134:135], v[110:111], s[26:27], v[228:229] op_sel_hi:[1,0,1]
	s_waitcnt vmcnt(8)
	v_pk_fma_f32 v[122:123], v[108:109], s[26:27], v[234:235] op_sel_hi:[1,0,1]
	v_pk_fma_f32 v[120:121], v[128:129], s[26:27], v[232:233] op_sel_hi:[1,0,1]
	v_cvt_pk_bf16_f32 v108, v134, v135
	v_cvt_pk_bf16_f32 v109, v112, v113
	v_mul_f32_e32 v116, v74, v134
	v_cvt_pk_bf16_f32 v110, v120, v121
	v_cvt_pk_bf16_f32 v111, v122, v123
	v_mul_f32_e32 v117, v75, v135
	v_mul_f32_e32 v118, v76, v112
	v_mul_f32_e32 v119, v77, v113
	v_mul_f32_e32 v128, v66, v120
	v_mul_f32_e32 v129, v67, v121
	v_mul_f32_e32 v136, v68, v122
	v_mul_f32_e32 v137, v69, v123
	global_store_dwordx4 v[130:131], v[108:111], off
	v_mul_f32_e32 v113, v113, v113
	v_fmac_f32_e32 v113, v112, v112
	v_mul_f32_e32 v108, 0x41c00000, v116
	v_mul_f32_e32 v109, 0x41c00000, v117
	v_mul_f32_e32 v110, 0x41c00000, v118
	v_mul_f32_e32 v111, 0x41c00000, v119
	v_mul_f32_e32 v116, 0x41c00000, v128
	v_mul_f32_e32 v117, 0x41c00000, v129
	v_mul_f32_e32 v118, 0x41c00000, v136
	v_mul_f32_e32 v119, 0x41c00000, v137
	v_med3_f32 v108, v108, s51, v177
	v_med3_f32 v109, v109, s51, v177
	v_med3_f32 v110, v110, s51, v177
	v_med3_f32 v111, v111, s51, v177
	v_med3_f32 v116, v116, s51, v177
	v_med3_f32 v117, v117, s51, v177
	v_med3_f32 v118, v118, s51, v177
	v_med3_f32 v119, v119, s51, v177
	v_add_f32_e32 v108, 0x4b400000, v108
	v_add_f32_e32 v109, 0x4b400000, v109
	v_add_f32_e32 v110, 0x4b400000, v110
	v_add_f32_e32 v111, 0x4b400000, v111
	v_add_f32_e32 v116, 0x4b400000, v116
	v_add_f32_e32 v117, 0x4b400000, v117
	v_add_f32_e32 v118, 0x4b400000, v118
	v_add_f32_e32 v119, 0x4b400000, v119
	v_perm_b32 v108, v109, v108, s56
	v_perm_b32 v109, v111, v110, s57
	v_perm_b32 v110, v117, v116, s56
	v_perm_b32 v111, v119, v118, s57
	v_or_b32_e32 v108, v108, v109
	v_or_b32_e32 v109, v110, v111
	global_store_dwordx2 v[106:107], v[108:109], off
	s_nop 0
	s_nop 0
	s_nop 0
	v_mul_f32_e32 v126, v135, v135
	v_fmac_f32_e32 v126, v134, v134
	v_mul_f32_e32 v121, v121, v121
	v_add_f32_e32 v112, v126, v113
	v_fmac_f32_e32 v121, v120, v120
	v_mul_f32_e32 v123, v123, v123
	v_fmac_f32_e32 v123, v122, v122
	v_add_f32_e32 v112, v112, v121
	v_add_f32_e32 v112, v123, v112
	s_waitcnt vmcnt(11)
; __device__ __forceinline__ unsigned cvt_pk_bf16(float lo, float hi) { unsigned r; asm volatile("v_cvt_pk_bf16_f32 %0, %1, %2" : "=v"(r) : "v"(lo), "v"(hi)); return r; }
;     __device__ __forceinline__ void operator()(const f32x4 (&acc)[2][2][4][2], const Unit& u, int wr, int wc, int fr, int fq) const {
;     ...
;             for (int m = 0; m < 4; ++m) { const size_t r = (size_t)(row0 + ai * HALF + m * 16); float ss = 0.f;
; #pragma unroll
;                 for (int bj = 0; bj < 2; ++bj) { const size_t off = r * 4096 + col0 + bj * HALF;
;                     const f32x4 v0 = acc[ai][bj][m][0] * scale + *(const f32x4*)(R + off), v1 = acc[ai][bj][m][1] * scale + *(const f32x4*)(R + off + 4);
;                     ss += (v0[0] * v0[0] + v0[1] * v0[1]) + (v0[2] * v0[2] + v0[3] * v0[3]) + (v1[0] * v1[0] + v1[1] * v1[1]) + (v1[2] * v1[2] + v1[3] * v1[3]);
;                     u32x4 w; w.x = cvt_pk_bf16(v0[0], v0[1]); w.y = cvt_pk_bf16(v0[2], v0[3]); w.z = cvt_pk_bf16(v1[0], v1[1]); w.w = cvt_pk_bf16(v1[2], v1[3]);
;                     *(u32x4*)(HB + off) = w;
;                     u32x2e q; q.x = q8x4(v0, gv[bj][0], (float)HQS); q.y = q8x4(v1, gv[bj][1], (float)HQS);
;                     *(u32x2e*)(Q8 + r * LDQ8 + col0 + bj * HALF) = q; }
;                 ss += __shfl_xor(ss, 16); ss += __shfl_xor(ss, 32);
;                 if (fq == 0) SSQP[r * 64 + u.pn * 4 + wc] = ss; }
	v_pk_fma_f32 v[104:105], v[104:105], s[26:27], v[238:239] op_sel_hi:[1,0,1]
	v_pk_fma_f32 v[102:103], v[102:103], s[26:27], v[236:237] op_sel_hi:[1,0,1]
	s_waitcnt vmcnt(11)
	v_pk_fma_f32 v[110:111], v[98:99], s[26:27], v[240:241] op_sel_hi:[1,0,1]
	v_mul_f32_e32 v113, v103, v103
	v_mul_f32_e32 v116, v105, v105
	v_pk_fma_f32 v[108:109], v[100:101], s[26:27], v[242:243] op_sel_hi:[1,0,1]
	v_mul_f32_e32 v117, v111, v111
	v_cvt_pk_bf16_f32 v98, v102, v103
	v_cvt_pk_bf16_f32 v99, v104, v105
	v_cvt_pk_bf16_f32 v100, v110, v111
	v_cvt_pk_bf16_f32 v101, v108, v109
	v_mul_f32_e32 v119, v62, v102
	v_mul_f32_e32 v103, v63, v103
	v_mul_f32_e32 v120, v64, v104
	v_mul_f32_e32 v105, v65, v105
	v_fmac_f32_e32 v113, v102, v102
	v_fmac_f32_e32 v116, v104, v104
	v_mul_f32_e32 v118, v109, v109
	v_fmac_f32_e32 v117, v110, v110
	global_store_dwordx4 v[124:125], v[98:101], off
	v_fmac_f32_e32 v118, v108, v108
	v_mul_f32_e32 v121, v50, v110
	v_mul_f32_e32 v98, 0x41c00000, v119
	v_mul_f32_e32 v99, 0x41c00000, v103
	v_mul_f32_e32 v100, 0x41c00000, v120
	v_mul_f32_e32 v101, 0x41c00000, v105
	v_add_f32_e32 v105, v113, v116
	v_med3_f32 v98, v98, s51, v177
	v_med3_f32 v99, v99, s51, v177
	v_med3_f32 v100, v100, s51, v177
	v_med3_f32 v101, v101, s51, v177
	v_add_f32_e32 v105, v105, v117
	v_add_f32_e32 v98, 0x4b400000, v98
	v_add_f32_e32 v99, 0x4b400000, v99
	v_add_f32_e32 v100, 0x4b400000, v100
	v_add_f32_e32 v101, 0x4b400000, v101
	v_add_f32_e32 v105, v118, v105
	v_perm_b32 v98, v99, v98, s56
	v_perm_b32 v99, v101, v100, s57
	v_add_f32_e32 v101, v112, v105
	v_or_b32_e32 v100, v98, v99
	ds_bpermute_b32 v98, v132, v101
	v_mul_f32_e32 v99, v53, v109
	v_mul_f32_e32 v99, 0x41c00000, v99
	v_mul_f32_e32 v111, v51, v111
	v_mul_f32_e32 v122, v52, v108
	v_med3_f32 v99, v99, s51, v177
	s_waitcnt lgkmcnt(0)
	v_add_f32_e32 v98, v101, v98
	v_mul_f32_e32 v102, 0x41c00000, v121
	v_mul_f32_e32 v103, 0x41c00000, v111
	v_mul_f32_e32 v104, 0x41c00000, v122
	v_add_f32_e32 v105, 0x4b400000, v99
	ds_bpermute_b32 v99, v133, v98
	v_med3_f32 v102, v102, s51, v177
	v_med3_f32 v103, v103, s51, v177
	v_med3_f32 v104, v104, s51, v177
	v_add_f32_e32 v102, 0x4b400000, v102
	v_add_f32_e32 v103, 0x4b400000, v103
	v_add_f32_e32 v104, 0x4b400000, v104
	v_perm_b32 v101, v103, v102, s56
	v_perm_b32 v102, v105, v104, s57
	v_or_b32_e32 v101, v101, v102
	global_store_dwordx2 v[106:107], v[100:101], off offset:128
	s_and_saveexec_b64 s[28:29], s[0:1]
	s_cbranch_execz .LBB0_623
	v_lshlrev_b64 v[100:101], 8, v[114:115]
	v_lshl_add_u64 v[100:101], s[22:23], 0, v[100:101]
	s_waitcnt lgkmcnt(0)
	v_add_f32_e32 v98, v98, v99
	global_store_dword v[100:101], v98, off
.LBB0_623:
	s_or_b64 exec, exec, s[28:29]
	s_add_u32 s98, s8, 0x200000
	s_addc_u32 s99, s9, 0
	global_load_dwordx4 v[228:231], v252, s[98:99]
	global_load_dwordx4 v[232:235], v252, s[98:99] offset:16
	global_load_dwordx4 v[236:239], v252, s[98:99] offset:512
	global_load_dwordx4 v[240:243], v252, s[98:99] offset:528
	v_or_b32_e32 v98, 48, v140
	s_waitcnt lgkmcnt(0)
	v_ashrrev_i32_e32 v99, 31, v98
	v_lshlrev_b64 v[100:101], 12, v[98:99]
	v_lshl_add_u64 v[108:109], v[100:101], 0, v[138:139]
	v_lshl_add_u64 v[110:111], v[108:109], 2, s[8:9]
	s_nop 0
	s_nop 0
	v_cvt_f32_i32_e32 v95, v95
	v_cvt_f32_i32_e32 v94, v94
	v_cvt_f32_i32_e32 v97, v97
	v_cvt_f32_i32_e32 v96, v96
	v_cvt_f32_i32_e32 v113, v91
	v_cvt_f32_i32_e32 v112, v90
	v_cvt_f32_i32_e32 v93, v93
	v_cvt_f32_i32_e32 v92, v92
	v_lshlrev_b64 v[108:109], 1, v[108:109]
	v_lshl_add_u64 v[114:115], s[14:15], 0, v[108:109]
	v_mad_i64_i32 v[90:91], s[28:29], v98, s50, v[142:143]
	v_cvt_f32_i32_e32 v87, v87
	v_cvt_f32_i32_e32 v86, v86
	v_cvt_f32_i32_e32 v89, v89
	v_cvt_f32_i32_e32 v88, v88
	v_cvt_f32_i32_e32 v83, v83
	v_cvt_f32_i32_e32 v82, v82
	v_cvt_f32_i32_e32 v85, v85
	v_cvt_f32_i32_e32 v84, v84
	v_or_b32_e32 v108, 0x100, v108
	v_lshl_add_u64 v[108:109], s[14:15], 0, v[108:109]
	s_waitcnt vmcnt(8)
	v_pk_fma_f32 v[96:97], v[96:97], s[26:27], v[214:215] op_sel_hi:[1,0,1]
	v_pk_fma_f32 v[116:117], v[94:95], s[26:27], v[212:213] op_sel_hi:[1,0,1]
	s_waitcnt vmcnt(8)
	v_pk_fma_f32 v[106:107], v[92:93], s[26:27], v[218:219] op_sel_hi:[1,0,1]
	v_pk_fma_f32 v[104:105], v[112:113], s[26:27], v[216:217] op_sel_hi:[1,0,1]
	v_cvt_pk_bf16_f32 v92, v116, v117
	v_cvt_pk_bf16_f32 v93, v96, v97
	v_mul_f32_e32 v100, v74, v116
	v_cvt_pk_bf16_f32 v94, v104, v105
	v_cvt_pk_bf16_f32 v95, v106, v107
	v_mul_f32_e32 v101, v75, v117
	v_mul_f32_e32 v102, v76, v96
	v_mul_f32_e32 v103, v77, v97
	v_mul_f32_e32 v112, v66, v104
	v_mul_f32_e32 v113, v67, v105
	v_mul_f32_e32 v118, v68, v106
	v_mul_f32_e32 v119, v69, v107
	global_store_dwordx4 v[114:115], v[92:95], off
	v_mul_f32_e32 v97, v97, v97
	v_fmac_f32_e32 v97, v96, v96
	v_mul_f32_e32 v92, 0x41c00000, v100
	v_mul_f32_e32 v93, 0x41c00000, v101
	v_mul_f32_e32 v94, 0x41c00000, v102
	v_mul_f32_e32 v95, 0x41c00000, v103
	v_mul_f32_e32 v100, 0x41c00000, v112
	v_mul_f32_e32 v101, 0x41c00000, v113
	v_mul_f32_e32 v102, 0x41c00000, v118
	v_mul_f32_e32 v103, 0x41c00000, v119
	v_med3_f32 v92, v92, s51, v177
	v_med3_f32 v93, v93, s51, v177
	v_med3_f32 v94, v94, s51, v177
	v_med3_f32 v95, v95, s51, v177
	v_med3_f32 v100, v100, s51, v177
	v_med3_f32 v101, v101, s51, v177
	v_med3_f32 v102, v102, s51, v177
	v_med3_f32 v103, v103, s51, v177
	v_add_f32_e32 v92, 0x4b400000, v92
	v_add_f32_e32 v93, 0x4b400000, v93
	v_add_f32_e32 v94, 0x4b400000, v94
	v_add_f32_e32 v95, 0x4b400000, v95
	v_add_f32_e32 v100, 0x4b400000, v100
	v_add_f32_e32 v101, 0x4b400000, v101
	v_add_f32_e32 v102, 0x4b400000, v102
	v_add_f32_e32 v103, 0x4b400000, v103
	v_perm_b32 v92, v93, v92, s56
	v_perm_b32 v93, v95, v94, s57
	v_perm_b32 v94, v101, v100, s56
	v_perm_b32 v95, v103, v102, s57
	v_or_b32_e32 v92, v92, v93
	v_or_b32_e32 v93, v94, v95
	global_store_dwordx2 v[90:91], v[92:93], off
	s_nop 0
	s_nop 0
	s_nop 0
	v_mul_f32_e32 v110, v117, v117
	v_fmac_f32_e32 v110, v116, v116
	v_mul_f32_e32 v105, v105, v105
	v_add_f32_e32 v96, v110, v97
	v_fmac_f32_e32 v105, v104, v104
	v_mul_f32_e32 v107, v107, v107
	v_fmac_f32_e32 v107, v106, v106
	v_add_f32_e32 v96, v96, v105
	v_add_f32_e32 v96, v107, v96
	s_waitcnt vmcnt(11)
; __device__ __forceinline__ unsigned cvt_pk_bf16(float lo, float hi) { unsigned r; asm volatile("v_cvt_pk_bf16_f32 %0, %1, %2" : "=v"(r) : "v"(lo), "v"(hi)); return r; }
;     __device__ __forceinline__ void operator()(const f32x4 (&acc)[2][2][4][2], const Unit& u, int wr, int wc, int fr, int fq) const {
;     ...
;             for (int m = 0; m < 4; ++m) { const size_t r = (size_t)(row0 + ai * HALF + m * 16); float ss = 0.f;
; #pragma unroll
;                 for (int bj = 0; bj < 2; ++bj) { const size_t off = r * 4096 + col0 + bj * HALF;
;                     const f32x4 v0 = acc[ai][bj][m][0] * scale + *(const f32x4*)(R + off), v1 = acc[ai][bj][m][1] * scale + *(const f32x4*)(R + off + 4);
;                     ss += (v0[0] * v0[0] + v0[1] * v0[1]) + (v0[2] * v0[2] + v0[3] * v0[3]) + (v1[0] * v1[0] + v1[1] * v1[1]) + (v1[2] * v1[2] + v1[3] * v1[3]);
;                     u32x4 w; w.x = cvt_pk_bf16(v0[0], v0[1]); w.y = cvt_pk_bf16(v0[2], v0[3]); w.z = cvt_pk_bf16(v1[0], v1[1]); w.w = cvt_pk_bf16(v1[2], v1[3]);
;                     *(u32x4*)(HB + off) = w;
;                     u32x2e q; q.x = q8x4(v0, gv[bj][0], (float)HQS); q.y = q8x4(v1, gv[bj][1], (float)HQS);
;                     *(u32x2e*)(Q8 + r * LDQ8 + col0 + bj * HALF) = q; }
;                 ss += __shfl_xor(ss, 16); ss += __shfl_xor(ss, 32);
;                 if (fq == 0) SSQP[r * 64 + u.pn * 4 + wc] = ss; }
	v_pk_fma_f32 v[88:89], v[88:89], s[26:27], v[222:223] op_sel_hi:[1,0,1]
	v_pk_fma_f32 v[86:87], v[86:87], s[26:27], v[220:221] op_sel_hi:[1,0,1]
	s_waitcnt vmcnt(11)
	v_pk_fma_f32 v[94:95], v[82:83], s[26:27], v[224:225] op_sel_hi:[1,0,1]
	v_mul_f32_e32 v97, v87, v87
	v_mul_f32_e32 v100, v89, v89
	v_pk_fma_f32 v[92:93], v[84:85], s[26:27], v[226:227] op_sel_hi:[1,0,1]
	v_mul_f32_e32 v101, v95, v95
	v_cvt_pk_bf16_f32 v82, v86, v87
	v_cvt_pk_bf16_f32 v83, v88, v89
	v_cvt_pk_bf16_f32 v84, v94, v95
	v_cvt_pk_bf16_f32 v85, v92, v93
	v_mul_f32_e32 v103, v62, v86
	v_mul_f32_e32 v87, v63, v87
	v_mul_f32_e32 v104, v64, v88
	v_mul_f32_e32 v89, v65, v89
	v_fmac_f32_e32 v97, v86, v86
	v_fmac_f32_e32 v100, v88, v88
	v_mul_f32_e32 v102, v93, v93
	v_fmac_f32_e32 v101, v94, v94
	global_store_dwordx4 v[108:109], v[82:85], off
	v_fmac_f32_e32 v102, v92, v92
	v_mul_f32_e32 v105, v50, v94
	v_mul_f32_e32 v82, 0x41c00000, v103
	v_mul_f32_e32 v83, 0x41c00000, v87
	v_mul_f32_e32 v84, 0x41c00000, v104
	v_mul_f32_e32 v85, 0x41c00000, v89
	v_add_f32_e32 v89, v97, v100
	v_med3_f32 v82, v82, s51, v177
	v_med3_f32 v83, v83, s51, v177
	v_med3_f32 v84, v84, s51, v177
	v_med3_f32 v85, v85, s51, v177
	v_add_f32_e32 v89, v89, v101
	v_add_f32_e32 v82, 0x4b400000, v82
	v_add_f32_e32 v83, 0x4b400000, v83
	v_add_f32_e32 v84, 0x4b400000, v84
	v_add_f32_e32 v85, 0x4b400000, v85
	v_add_f32_e32 v89, v102, v89
	v_perm_b32 v82, v83, v82, s56
	v_perm_b32 v83, v85, v84, s57
	v_add_f32_e32 v85, v96, v89
	v_or_b32_e32 v84, v82, v83
	ds_bpermute_b32 v82, v132, v85
	v_mul_f32_e32 v83, v53, v93
	v_mul_f32_e32 v83, 0x41c00000, v83
	v_mul_f32_e32 v95, v51, v95
	v_mul_f32_e32 v106, v52, v92
	v_med3_f32 v83, v83, s51, v177
	s_waitcnt lgkmcnt(0)
	v_add_f32_e32 v82, v85, v82
	v_mul_f32_e32 v86, 0x41c00000, v105
	v_mul_f32_e32 v87, 0x41c00000, v95
	v_mul_f32_e32 v88, 0x41c00000, v106
	v_add_f32_e32 v89, 0x4b400000, v83
	ds_bpermute_b32 v83, v133, v82
	v_med3_f32 v86, v86, s51, v177
	v_med3_f32 v87, v87, s51, v177
	v_med3_f32 v88, v88, s51, v177
	v_add_f32_e32 v86, 0x4b400000, v86
	v_add_f32_e32 v87, 0x4b400000, v87
	v_add_f32_e32 v88, 0x4b400000, v88
	v_perm_b32 v85, v87, v86, s56
	v_perm_b32 v86, v89, v88, s57
	v_or_b32_e32 v85, v85, v86
	global_store_dwordx2 v[90:91], v[84:85], off offset:128
	s_and_saveexec_b64 s[28:29], s[0:1]
	s_cbranch_execz .LBB0_625
	v_lshlrev_b64 v[84:85], 8, v[98:99]
	v_lshl_add_u64 v[84:85], s[22:23], 0, v[84:85]
	s_waitcnt lgkmcnt(0)
	v_add_f32_e32 v82, v82, v83
	global_store_dword v[84:85], v82, off
.LBB0_625:
	s_or_b64 exec, exec, s[28:29]
	s_add_u32 s98, s8, 0x240000
	s_addc_u32 s99, s9, 0
	global_load_dwordx4 v[212:215], v252, s[98:99]
	global_load_dwordx4 v[216:219], v252, s[98:99] offset:16
	global_load_dwordx4 v[220:223], v252, s[98:99] offset:512
	global_load_dwordx4 v[224:227], v252, s[98:99] offset:528
	v_add_u32_e32 v82, 0x80, v140
	s_waitcnt lgkmcnt(0)
	v_ashrrev_i32_e32 v83, 31, v82
	v_lshlrev_b64 v[84:85], 12, v[82:83]
	v_lshl_add_u64 v[92:93], v[84:85], 0, v[138:139]
	v_lshl_add_u64 v[94:95], v[92:93], 2, s[8:9]
	s_nop 0
	s_nop 0
	v_cvt_f32_i32_e32 v79, v79
	v_cvt_f32_i32_e32 v78, v78
	v_cvt_f32_i32_e32 v81, v81
	v_cvt_f32_i32_e32 v80, v80
	v_cvt_f32_i32_e32 v97, v71
	v_cvt_f32_i32_e32 v96, v70
	v_cvt_f32_i32_e32 v73, v73
	v_cvt_f32_i32_e32 v72, v72
	v_lshlrev_b64 v[92:93], 1, v[92:93]
	v_lshl_add_u64 v[98:99], s[14:15], 0, v[92:93]
	v_mad_i64_i32 v[70:71], s[28:29], v82, s50, v[142:143]
	v_cvt_f32_i32_e32 v59, v59
	v_cvt_f32_i32_e32 v58, v58
	v_cvt_f32_i32_e32 v61, v61
	v_cvt_f32_i32_e32 v60, v60
	v_cvt_f32_i32_e32 v55, v55
	v_cvt_f32_i32_e32 v54, v54
	v_or_b32_e32 v92, 0x100, v92
	v_cvt_f32_i32_e32 v57, v57
	v_cvt_f32_i32_e32 v56, v56
	s_waitcnt vmcnt(8)
	v_pk_fma_f32 v[100:101], v[80:81], s[26:27], v[230:231] op_sel_hi:[1,0,1]
	v_pk_fma_f32 v[102:103], v[78:79], s[26:27], v[228:229] op_sel_hi:[1,0,1]
	s_waitcnt vmcnt(8)
	v_pk_fma_f32 v[72:73], v[72:73], s[26:27], v[234:235] op_sel_hi:[1,0,1]
	v_pk_fma_f32 v[88:89], v[96:97], s[26:27], v[232:233] op_sel_hi:[1,0,1]
	v_cvt_pk_bf16_f32 v78, v102, v103
	v_cvt_pk_bf16_f32 v79, v100, v101
	v_mul_f32_e32 v84, v74, v102
	v_cvt_pk_bf16_f32 v80, v88, v89
	v_cvt_pk_bf16_f32 v81, v72, v73
	v_mul_f32_e32 v85, v75, v103
	v_mul_f32_e32 v86, v76, v100
	v_mul_f32_e32 v87, v77, v101
	v_mul_f32_e32 v90, v66, v88
	v_mul_f32_e32 v91, v67, v89
	v_mul_f32_e32 v96, v68, v72
	v_mul_f32_e32 v97, v69, v73
	global_store_dwordx4 v[98:99], v[78:81], off
	v_mul_f32_e32 v89, v89, v89
	v_mul_f32_e32 v73, v73, v73
	v_mul_f32_e32 v78, 0x41c00000, v84
	v_mul_f32_e32 v79, 0x41c00000, v85
	v_mul_f32_e32 v80, 0x41c00000, v86
	v_mul_f32_e32 v81, 0x41c00000, v87
	v_mul_f32_e32 v84, 0x41c00000, v90
	v_mul_f32_e32 v85, 0x41c00000, v91
	v_mul_f32_e32 v86, 0x41c00000, v96
	v_mul_f32_e32 v87, 0x41c00000, v97
	v_med3_f32 v78, v78, s51, v177
	v_med3_f32 v79, v79, s51, v177
	v_med3_f32 v80, v80, s51, v177
	v_med3_f32 v81, v81, s51, v177
	v_med3_f32 v84, v84, s51, v177
	v_med3_f32 v85, v85, s51, v177
	v_med3_f32 v86, v86, s51, v177
	v_med3_f32 v87, v87, s51, v177
	v_add_f32_e32 v78, 0x4b400000, v78
	v_add_f32_e32 v79, 0x4b400000, v79
	v_add_f32_e32 v80, 0x4b400000, v80
	v_add_f32_e32 v81, 0x4b400000, v81
	v_add_f32_e32 v84, 0x4b400000, v84
	v_add_f32_e32 v85, 0x4b400000, v85
	v_add_f32_e32 v86, 0x4b400000, v86
	v_add_f32_e32 v87, 0x4b400000, v87
	v_perm_b32 v78, v79, v78, s56
	v_perm_b32 v79, v81, v80, s57
	v_perm_b32 v80, v85, v84, s56
	v_perm_b32 v81, v87, v86, s57
	v_or_b32_e32 v78, v78, v79
	v_or_b32_e32 v79, v80, v81
	global_store_dwordx2 v[70:71], v[78:79], off
	s_nop 0
	s_nop 0
	s_nop 0
	v_lshl_add_u64 v[90:91], s[14:15], 0, v[92:93]
	v_mul_f32_e32 v92, v103, v103
	v_mul_f32_e32 v93, v101, v101
	v_fmac_f32_e32 v92, v102, v102
	v_fmac_f32_e32 v93, v100, v100
	v_fmac_f32_e32 v89, v88, v88
	v_fmac_f32_e32 v73, v72, v72
	v_add_f32_e32 v72, v92, v93
	v_add_f32_e32 v72, v72, v89
	v_add_f32_e32 v88, v73, v72
	s_waitcnt vmcnt(11)
; __device__ __forceinline__ unsigned cvt_pk_bf16(float lo, float hi) { unsigned r; asm volatile("v_cvt_pk_bf16_f32 %0, %1, %2" : "=v"(r) : "v"(lo), "v"(hi)); return r; }
;     __device__ __forceinline__ void operator()(const f32x4 (&acc)[2][2][4][2], const Unit& u, int wr, int wc, int fr, int fq) const {
;     ...
;             for (int m = 0; m < 4; ++m) { const size_t r = (size_t)(row0 + ai * HALF + m * 16); float ss = 0.f;
; #pragma unroll
;                 for (int bj = 0; bj < 2; ++bj) { const size_t off = r * 4096 + col0 + bj * HALF;
;                     const f32x4 v0 = acc[ai][bj][m][0] * scale + *(const f32x4*)(R + off), v1 = acc[ai][bj][m][1] * scale + *(const f32x4*)(R + off + 4);
;                     ss += (v0[0] * v0[0] + v0[1] * v0[1]) + (v0[2] * v0[2] + v0[3] * v0[3]) + (v1[0] * v1[0] + v1[1] * v1[1]) + (v1[2] * v1[2] + v1[3] * v1[3]);
;                     u32x4 w; w.x = cvt_pk_bf16(v0[0], v0[1]); w.y = cvt_pk_bf16(v0[2], v0[3]); w.z = cvt_pk_bf16(v1[0], v1[1]); w.w = cvt_pk_bf16(v1[2], v1[3]);
;                     *(u32x4*)(HB + off) = w;
;                     u32x2e q; q.x = q8x4(v0, gv[bj][0], (float)HQS); q.y = q8x4(v1, gv[bj][1], (float)HQS);
;                     *(u32x2e*)(Q8 + r * LDQ8 + col0 + bj * HALF) = q; }
;                 ss += __shfl_xor(ss, 16); ss += __shfl_xor(ss, 32);
;                 if (fq == 0) SSQP[r * 64 + u.pn * 4 + wc] = ss; }
	v_pk_fma_f32 v[60:61], v[60:61], s[26:27], v[238:239] op_sel_hi:[1,0,1]
	v_pk_fma_f32 v[58:59], v[58:59], s[26:27], v[236:237] op_sel_hi:[1,0,1]
	s_waitcnt vmcnt(11)
	v_pk_fma_f32 v[78:79], v[54:55], s[26:27], v[240:241] op_sel_hi:[1,0,1]
	v_mul_f32_e32 v80, v59, v59
	v_mul_f32_e32 v81, v61, v61
	v_pk_fma_f32 v[72:73], v[56:57], s[26:27], v[242:243] op_sel_hi:[1,0,1]
	v_mul_f32_e32 v84, v79, v79
	v_cvt_pk_bf16_f32 v54, v58, v59
	v_cvt_pk_bf16_f32 v55, v60, v61
	v_cvt_pk_bf16_f32 v56, v78, v79
	v_cvt_pk_bf16_f32 v57, v72, v73
	v_mul_f32_e32 v86, v62, v58
	v_mul_f32_e32 v59, v63, v59
	v_mul_f32_e32 v87, v64, v60
	v_mul_f32_e32 v61, v65, v61
	v_fmac_f32_e32 v80, v58, v58
	v_fmac_f32_e32 v81, v60, v60
	v_mul_f32_e32 v85, v73, v73
	v_fmac_f32_e32 v84, v78, v78
	global_store_dwordx4 v[90:91], v[54:57], off
	v_fmac_f32_e32 v85, v72, v72
	v_mul_f32_e32 v89, v50, v78
	v_mul_f32_e32 v54, 0x41c00000, v86
	v_mul_f32_e32 v55, 0x41c00000, v59
	v_mul_f32_e32 v56, 0x41c00000, v87
	v_mul_f32_e32 v57, 0x41c00000, v61
	v_add_f32_e32 v61, v80, v81
	v_med3_f32 v54, v54, s51, v177
	v_med3_f32 v55, v55, s51, v177
	v_med3_f32 v56, v56, s51, v177
	v_med3_f32 v57, v57, s51, v177
	v_add_f32_e32 v61, v61, v84
	v_add_f32_e32 v54, 0x4b400000, v54
	v_add_f32_e32 v55, 0x4b400000, v55
	v_add_f32_e32 v56, 0x4b400000, v56
	v_add_f32_e32 v57, 0x4b400000, v57
	v_add_f32_e32 v61, v85, v61
	v_perm_b32 v54, v55, v54, s56
	v_perm_b32 v55, v57, v56, s57
	v_add_f32_e32 v57, v88, v61
	v_or_b32_e32 v56, v54, v55
	ds_bpermute_b32 v54, v132, v57
	v_mul_f32_e32 v55, v53, v73
	v_mul_f32_e32 v55, 0x41c00000, v55
	v_mul_f32_e32 v79, v51, v79
	v_mul_f32_e32 v92, v52, v72
	v_med3_f32 v55, v55, s51, v177
	s_waitcnt lgkmcnt(0)
	v_add_f32_e32 v54, v57, v54
	v_mul_f32_e32 v58, 0x41c00000, v89
	v_mul_f32_e32 v59, 0x41c00000, v79
	v_mul_f32_e32 v60, 0x41c00000, v92
	v_add_f32_e32 v61, 0x4b400000, v55
	ds_bpermute_b32 v55, v133, v54
	v_med3_f32 v58, v58, s51, v177
	v_med3_f32 v59, v59, s51, v177
	v_med3_f32 v60, v60, s51, v177
	v_add_f32_e32 v58, 0x4b400000, v58
	v_add_f32_e32 v59, 0x4b400000, v59
	v_add_f32_e32 v60, 0x4b400000, v60
	v_perm_b32 v57, v59, v58, s56
	v_perm_b32 v58, v61, v60, s57
	v_or_b32_e32 v57, v57, v58
	global_store_dwordx2 v[70:71], v[56:57], off offset:128
	s_and_saveexec_b64 s[28:29], s[0:1]
	s_cbranch_execz .LBB0_627
	v_lshlrev_b64 v[56:57], 8, v[82:83]
	v_lshl_add_u64 v[56:57], s[22:23], 0, v[56:57]
	s_waitcnt lgkmcnt(0)
	v_add_f32_e32 v54, v54, v55
	global_store_dword v[56:57], v54, off
.LBB0_627:
	s_or_b64 exec, exec, s[28:29]
	s_add_u32 s98, s8, 0x280000
	s_addc_u32 s99, s9, 0
	global_load_dwordx4 v[228:231], v252, s[98:99]
	global_load_dwordx4 v[232:235], v252, s[98:99] offset:16
	global_load_dwordx4 v[236:239], v252, s[98:99] offset:512
	global_load_dwordx4 v[240:243], v252, s[98:99] offset:528
	v_add_u32_e32 v54, 0x90, v140
	s_waitcnt lgkmcnt(0)
	v_ashrrev_i32_e32 v55, 31, v54
	v_lshlrev_b64 v[56:57], 12, v[54:55]
	v_lshl_add_u64 v[60:61], v[56:57], 0, v[138:139]
	v_lshl_add_u64 v[78:79], v[60:61], 2, s[8:9]
	s_nop 0
	s_nop 0
	v_cvt_f32_i32_e32 v47, v47
	v_cvt_f32_i32_e32 v46, v46
	v_cvt_f32_i32_e32 v49, v49
	v_cvt_f32_i32_e32 v48, v48
	v_cvt_f32_i32_e32 v81, v43
	v_cvt_f32_i32_e32 v80, v42
	v_cvt_f32_i32_e32 v45, v45
	v_cvt_f32_i32_e32 v44, v44
	v_lshlrev_b64 v[60:61], 1, v[60:61]
	v_lshl_add_u64 v[82:83], s[14:15], 0, v[60:61]
	v_mad_i64_i32 v[42:43], s[28:29], v54, s50, v[142:143]
	v_cvt_f32_i32_e32 v39, v39
	v_cvt_f32_i32_e32 v38, v38
	v_cvt_f32_i32_e32 v41, v41
	v_cvt_f32_i32_e32 v40, v40
	v_cvt_f32_i32_e32 v35, v35
	v_cvt_f32_i32_e32 v34, v34
	v_cvt_f32_i32_e32 v37, v37
	v_cvt_f32_i32_e32 v36, v36
	v_or_b32_e32 v60, 0x100, v60
	v_lshl_add_u64 v[60:61], s[14:15], 0, v[60:61]
	s_waitcnt vmcnt(8)
	v_pk_fma_f32 v[48:49], v[48:49], s[26:27], v[214:215] op_sel_hi:[1,0,1]
	v_pk_fma_f32 v[84:85], v[46:47], s[26:27], v[212:213] op_sel_hi:[1,0,1]
	s_waitcnt vmcnt(8)
	v_pk_fma_f32 v[72:73], v[44:45], s[26:27], v[218:219] op_sel_hi:[1,0,1]
	v_pk_fma_f32 v[70:71], v[80:81], s[26:27], v[216:217] op_sel_hi:[1,0,1]
	v_cvt_pk_bf16_f32 v44, v84, v85
	v_cvt_pk_bf16_f32 v45, v48, v49
	v_mul_f32_e32 v56, v74, v84
	v_cvt_pk_bf16_f32 v46, v70, v71
	v_cvt_pk_bf16_f32 v47, v72, v73
	v_mul_f32_e32 v57, v75, v85
	v_mul_f32_e32 v58, v76, v48
	v_mul_f32_e32 v59, v77, v49
	v_mul_f32_e32 v80, v66, v70
	v_mul_f32_e32 v81, v67, v71
	v_mul_f32_e32 v86, v68, v72
	v_mul_f32_e32 v87, v69, v73
	global_store_dwordx4 v[82:83], v[44:47], off
	v_mul_f32_e32 v49, v49, v49
	v_fmac_f32_e32 v49, v48, v48
	v_mul_f32_e32 v44, 0x41c00000, v56
	v_mul_f32_e32 v45, 0x41c00000, v57
	v_mul_f32_e32 v46, 0x41c00000, v58
	v_mul_f32_e32 v47, 0x41c00000, v59
	v_mul_f32_e32 v56, 0x41c00000, v80
	v_mul_f32_e32 v57, 0x41c00000, v81
	v_mul_f32_e32 v58, 0x41c00000, v86
	v_mul_f32_e32 v59, 0x41c00000, v87
	v_med3_f32 v44, v44, s51, v177
	v_med3_f32 v45, v45, s51, v177
	v_med3_f32 v46, v46, s51, v177
	v_med3_f32 v47, v47, s51, v177
	v_med3_f32 v56, v56, s51, v177
	v_med3_f32 v57, v57, s51, v177
	v_med3_f32 v58, v58, s51, v177
	v_med3_f32 v59, v59, s51, v177
	v_add_f32_e32 v44, 0x4b400000, v44
	v_add_f32_e32 v45, 0x4b400000, v45
	v_add_f32_e32 v46, 0x4b400000, v46
	v_add_f32_e32 v47, 0x4b400000, v47
	v_add_f32_e32 v56, 0x4b400000, v56
	v_add_f32_e32 v57, 0x4b400000, v57
	v_add_f32_e32 v58, 0x4b400000, v58
	v_add_f32_e32 v59, 0x4b400000, v59
	v_perm_b32 v44, v45, v44, s56
	v_perm_b32 v45, v47, v46, s57
	v_perm_b32 v46, v57, v56, s56
	v_perm_b32 v47, v59, v58, s57
	v_or_b32_e32 v44, v44, v45
	v_or_b32_e32 v45, v46, v47
	global_store_dwordx2 v[42:43], v[44:45], off
	s_nop 0
	s_nop 0
	s_nop 0
	v_mul_f32_e32 v78, v85, v85
	v_fmac_f32_e32 v78, v84, v84
	v_mul_f32_e32 v71, v71, v71
	v_add_f32_e32 v48, v78, v49
	v_fmac_f32_e32 v71, v70, v70
	v_mul_f32_e32 v73, v73, v73
	v_fmac_f32_e32 v73, v72, v72
	v_add_f32_e32 v48, v48, v71
	v_add_f32_e32 v48, v73, v48
	s_waitcnt vmcnt(11)
; __device__ __forceinline__ unsigned cvt_pk_bf16(float lo, float hi) { unsigned r; asm volatile("v_cvt_pk_bf16_f32 %0, %1, %2" : "=v"(r) : "v"(lo), "v"(hi)); return r; }
;     __device__ __forceinline__ void operator()(const f32x4 (&acc)[2][2][4][2], const Unit& u, int wr, int wc, int fr, int fq) const {
;     ...
;             for (int m = 0; m < 4; ++m) { const size_t r = (size_t)(row0 + ai * HALF + m * 16); float ss = 0.f;
; #pragma unroll
;                 for (int bj = 0; bj < 2; ++bj) { const size_t off = r * 4096 + col0 + bj * HALF;
;                     const f32x4 v0 = acc[ai][bj][m][0] * scale + *(const f32x4*)(R + off), v1 = acc[ai][bj][m][1] * scale + *(const f32x4*)(R + off + 4);
;                     ss += (v0[0] * v0[0] + v0[1] * v0[1]) + (v0[2] * v0[2] + v0[3] * v0[3]) + (v1[0] * v1[0] + v1[1] * v1[1]) + (v1[2] * v1[2] + v1[3] * v1[3]);
;                     u32x4 w; w.x = cvt_pk_bf16(v0[0], v0[1]); w.y = cvt_pk_bf16(v0[2], v0[3]); w.z = cvt_pk_bf16(v1[0], v1[1]); w.w = cvt_pk_bf16(v1[2], v1[3]);
;                     *(u32x4*)(HB + off) = w;
;                     u32x2e q; q.x = q8x4(v0, gv[bj][0], (float)HQS); q.y = q8x4(v1, gv[bj][1], (float)HQS);
;                     *(u32x2e*)(Q8 + r * LDQ8 + col0 + bj * HALF) = q; }
;                 ss += __shfl_xor(ss, 16); ss += __shfl_xor(ss, 32);
;                 if (fq == 0) SSQP[r * 64 + u.pn * 4 + wc] = ss; }
	v_pk_fma_f32 v[40:41], v[40:41], s[26:27], v[222:223] op_sel_hi:[1,0,1]
	v_pk_fma_f32 v[38:39], v[38:39], s[26:27], v[220:221] op_sel_hi:[1,0,1]
	s_waitcnt vmcnt(11)
	v_pk_fma_f32 v[46:47], v[34:35], s[26:27], v[224:225] op_sel_hi:[1,0,1]
	v_mul_f32_e32 v49, v39, v39
	v_mul_f32_e32 v56, v41, v41
	v_pk_fma_f32 v[44:45], v[36:37], s[26:27], v[226:227] op_sel_hi:[1,0,1]
	v_mul_f32_e32 v57, v47, v47
	v_cvt_pk_bf16_f32 v34, v38, v39
	v_cvt_pk_bf16_f32 v35, v40, v41
	v_cvt_pk_bf16_f32 v36, v46, v47
	v_cvt_pk_bf16_f32 v37, v44, v45
	v_mul_f32_e32 v59, v62, v38
	v_mul_f32_e32 v39, v63, v39
	v_mul_f32_e32 v70, v64, v40
	v_mul_f32_e32 v41, v65, v41
	v_fmac_f32_e32 v49, v38, v38
	v_fmac_f32_e32 v56, v40, v40
	v_mul_f32_e32 v58, v45, v45
	v_fmac_f32_e32 v57, v46, v46
	global_store_dwordx4 v[60:61], v[34:37], off
	v_fmac_f32_e32 v58, v44, v44
	v_mul_f32_e32 v71, v50, v46
	v_mul_f32_e32 v34, 0x41c00000, v59
	v_mul_f32_e32 v35, 0x41c00000, v39
	v_mul_f32_e32 v36, 0x41c00000, v70
	v_mul_f32_e32 v37, 0x41c00000, v41
	v_add_f32_e32 v41, v49, v56
	v_med3_f32 v34, v34, s51, v177
	v_med3_f32 v35, v35, s51, v177
	v_med3_f32 v36, v36, s51, v177
	v_med3_f32 v37, v37, s51, v177
	v_add_f32_e32 v41, v41, v57
	v_add_f32_e32 v34, 0x4b400000, v34
	v_add_f32_e32 v35, 0x4b400000, v35
	v_add_f32_e32 v36, 0x4b400000, v36
	v_add_f32_e32 v37, 0x4b400000, v37
	v_add_f32_e32 v41, v58, v41
	v_perm_b32 v34, v35, v34, s56
	v_perm_b32 v35, v37, v36, s57
	v_add_f32_e32 v37, v48, v41
	v_or_b32_e32 v36, v34, v35
	ds_bpermute_b32 v34, v132, v37
	v_mul_f32_e32 v35, v53, v45
	v_mul_f32_e32 v35, 0x41c00000, v35
	v_mul_f32_e32 v47, v51, v47
	v_mul_f32_e32 v72, v52, v44
	v_med3_f32 v35, v35, s51, v177
	s_waitcnt lgkmcnt(0)
	v_add_f32_e32 v34, v37, v34
	v_mul_f32_e32 v38, 0x41c00000, v71
	v_mul_f32_e32 v39, 0x41c00000, v47
	v_mul_f32_e32 v40, 0x41c00000, v72
	v_add_f32_e32 v41, 0x4b400000, v35
	ds_bpermute_b32 v35, v133, v34
	v_med3_f32 v38, v38, s51, v177
	v_med3_f32 v39, v39, s51, v177
	v_med3_f32 v40, v40, s51, v177
	v_add_f32_e32 v38, 0x4b400000, v38
	v_add_f32_e32 v39, 0x4b400000, v39
	v_add_f32_e32 v40, 0x4b400000, v40
	v_perm_b32 v37, v39, v38, s56
	v_perm_b32 v38, v41, v40, s57
	v_or_b32_e32 v37, v37, v38
	global_store_dwordx2 v[42:43], v[36:37], off offset:128
	s_and_saveexec_b64 s[28:29], s[0:1]
	s_cbranch_execz .LBB0_629
	v_lshlrev_b64 v[36:37], 8, v[54:55]
	v_lshl_add_u64 v[36:37], s[22:23], 0, v[36:37]
	s_waitcnt lgkmcnt(0)
	v_add_f32_e32 v34, v34, v35
	global_store_dword v[36:37], v34, off
.LBB0_629:
	s_or_b64 exec, exec, s[28:29]
	s_add_u32 s98, s8, 0x2c0000
	s_addc_u32 s99, s9, 0
	global_load_dwordx4 v[212:215], v252, s[98:99]
	global_load_dwordx4 v[216:219], v252, s[98:99] offset:16
	global_load_dwordx4 v[220:223], v252, s[98:99] offset:512
	global_load_dwordx4 v[224:227], v252, s[98:99] offset:528
	v_add_u32_e32 v34, 0xa0, v140
	s_waitcnt lgkmcnt(0)
	v_ashrrev_i32_e32 v35, 31, v34
	v_lshlrev_b64 v[36:37], 12, v[34:35]
	v_lshl_add_u64 v[44:45], v[36:37], 0, v[138:139]
	v_lshl_add_u64 v[46:47], v[44:45], 2, s[8:9]
	s_nop 0
	s_nop 0
	v_cvt_f32_i32_e32 v31, v31
	v_cvt_f32_i32_e32 v30, v30
	v_cvt_f32_i32_e32 v33, v33
	v_cvt_f32_i32_e32 v32, v32
	v_cvt_f32_i32_e32 v49, v27
	v_cvt_f32_i32_e32 v48, v26
	v_cvt_f32_i32_e32 v29, v29
	v_cvt_f32_i32_e32 v28, v28
	v_lshlrev_b64 v[44:45], 1, v[44:45]
	v_lshl_add_u64 v[54:55], s[14:15], 0, v[44:45]
	v_mad_i64_i32 v[26:27], s[28:29], v34, s50, v[142:143]
	v_cvt_f32_i32_e32 v23, v23
	v_cvt_f32_i32_e32 v22, v22
	v_cvt_f32_i32_e32 v25, v25
	v_cvt_f32_i32_e32 v24, v24
	v_cvt_f32_i32_e32 v19, v19
	v_cvt_f32_i32_e32 v18, v18
	v_cvt_f32_i32_e32 v21, v21
	v_cvt_f32_i32_e32 v20, v20
	v_or_b32_e32 v44, 0x100, v44
	v_lshl_add_u64 v[44:45], s[14:15], 0, v[44:45]
	s_waitcnt vmcnt(8)
	v_pk_fma_f32 v[32:33], v[32:33], s[26:27], v[230:231] op_sel_hi:[1,0,1]
	v_pk_fma_f32 v[56:57], v[30:31], s[26:27], v[228:229] op_sel_hi:[1,0,1]
	s_waitcnt vmcnt(8)
	v_pk_fma_f32 v[42:43], v[28:29], s[26:27], v[234:235] op_sel_hi:[1,0,1]
	v_pk_fma_f32 v[40:41], v[48:49], s[26:27], v[232:233] op_sel_hi:[1,0,1]
	v_cvt_pk_bf16_f32 v28, v56, v57
	v_cvt_pk_bf16_f32 v29, v32, v33
	v_mul_f32_e32 v36, v74, v56
	v_cvt_pk_bf16_f32 v30, v40, v41
	v_cvt_pk_bf16_f32 v31, v42, v43
	v_mul_f32_e32 v37, v75, v57
	v_mul_f32_e32 v38, v76, v32
	v_mul_f32_e32 v39, v77, v33
	v_mul_f32_e32 v48, v66, v40
	v_mul_f32_e32 v49, v67, v41
	v_mul_f32_e32 v58, v68, v42
	v_mul_f32_e32 v59, v69, v43
	global_store_dwordx4 v[54:55], v[28:31], off
	v_mul_f32_e32 v33, v33, v33
	v_fmac_f32_e32 v33, v32, v32
	v_mul_f32_e32 v28, 0x41c00000, v36
	v_mul_f32_e32 v29, 0x41c00000, v37
	v_mul_f32_e32 v30, 0x41c00000, v38
	v_mul_f32_e32 v31, 0x41c00000, v39
	v_mul_f32_e32 v36, 0x41c00000, v48
	v_mul_f32_e32 v37, 0x41c00000, v49
	v_mul_f32_e32 v38, 0x41c00000, v58
	v_mul_f32_e32 v39, 0x41c00000, v59
	v_med3_f32 v28, v28, s51, v177
	v_med3_f32 v29, v29, s51, v177
	v_med3_f32 v30, v30, s51, v177
	v_med3_f32 v31, v31, s51, v177
	v_med3_f32 v36, v36, s51, v177
	v_med3_f32 v37, v37, s51, v177
	v_med3_f32 v38, v38, s51, v177
	v_med3_f32 v39, v39, s51, v177
	v_add_f32_e32 v28, 0x4b400000, v28
	v_add_f32_e32 v29, 0x4b400000, v29
	v_add_f32_e32 v30, 0x4b400000, v30
	v_add_f32_e32 v31, 0x4b400000, v31
	v_add_f32_e32 v36, 0x4b400000, v36
	v_add_f32_e32 v37, 0x4b400000, v37
	v_add_f32_e32 v38, 0x4b400000, v38
	v_add_f32_e32 v39, 0x4b400000, v39
	v_perm_b32 v28, v29, v28, s56
	v_perm_b32 v29, v31, v30, s57
	v_perm_b32 v30, v37, v36, s56
	v_perm_b32 v31, v39, v38, s57
	v_or_b32_e32 v28, v28, v29
	v_or_b32_e32 v29, v30, v31
	global_store_dwordx2 v[26:27], v[28:29], off
	s_nop 0
	s_nop 0
	s_nop 0
	v_mul_f32_e32 v46, v57, v57
	v_fmac_f32_e32 v46, v56, v56
	v_mul_f32_e32 v41, v41, v41
	v_add_f32_e32 v32, v46, v33
	v_fmac_f32_e32 v41, v40, v40
	v_mul_f32_e32 v43, v43, v43
	v_fmac_f32_e32 v43, v42, v42
	v_add_f32_e32 v32, v32, v41
	v_add_f32_e32 v32, v43, v32
	s_waitcnt vmcnt(11)
; __device__ __forceinline__ unsigned cvt_pk_bf16(float lo, float hi) { unsigned r; asm volatile("v_cvt_pk_bf16_f32 %0, %1, %2" : "=v"(r) : "v"(lo), "v"(hi)); return r; }
;     __device__ __forceinline__ void operator()(const f32x4 (&acc)[2][2][4][2], const Unit& u, int wr, int wc, int fr, int fq) const {
;     ...
;             for (int m = 0; m < 4; ++m) { const size_t r = (size_t)(row0 + ai * HALF + m * 16); float ss = 0.f;
; #pragma unroll
;                 for (int bj = 0; bj < 2; ++bj) { const size_t off = r * 4096 + col0 + bj * HALF;
;                     const f32x4 v0 = acc[ai][bj][m][0] * scale + *(const f32x4*)(R + off), v1 = acc[ai][bj][m][1] * scale + *(const f32x4*)(R + off + 4);
;                     ss += (v0[0] * v0[0] + v0[1] * v0[1]) + (v0[2] * v0[2] + v0[3] * v0[3]) + (v1[0] * v1[0] + v1[1] * v1[1]) + (v1[2] * v1[2] + v1[3] * v1[3]);
;                     u32x4 w; w.x = cvt_pk_bf16(v0[0], v0[1]); w.y = cvt_pk_bf16(v0[2], v0[3]); w.z = cvt_pk_bf16(v1[0], v1[1]); w.w = cvt_pk_bf16(v1[2], v1[3]);
;                     *(u32x4*)(HB + off) = w;
;                     u32x2e q; q.x = q8x4(v0, gv[bj][0], (float)HQS); q.y = q8x4(v1, gv[bj][1], (float)HQS);
;                     *(u32x2e*)(Q8 + r * LDQ8 + col0 + bj * HALF) = q; }
;                 ss += __shfl_xor(ss, 16); ss += __shfl_xor(ss, 32);
;                 if (fq == 0) SSQP[r * 64 + u.pn * 4 + wc] = ss; }
	v_pk_fma_f32 v[24:25], v[24:25], s[26:27], v[238:239] op_sel_hi:[1,0,1]
	v_pk_fma_f32 v[22:23], v[22:23], s[26:27], v[236:237] op_sel_hi:[1,0,1]
	s_waitcnt vmcnt(11)
	v_pk_fma_f32 v[30:31], v[18:19], s[26:27], v[240:241] op_sel_hi:[1,0,1]
	v_mul_f32_e32 v33, v23, v23
	v_mul_f32_e32 v36, v25, v25
	v_pk_fma_f32 v[28:29], v[20:21], s[26:27], v[242:243] op_sel_hi:[1,0,1]
	v_mul_f32_e32 v37, v31, v31
	v_cvt_pk_bf16_f32 v18, v22, v23
	v_cvt_pk_bf16_f32 v19, v24, v25
	v_cvt_pk_bf16_f32 v20, v30, v31
	v_cvt_pk_bf16_f32 v21, v28, v29
	v_mul_f32_e32 v39, v62, v22
	v_mul_f32_e32 v23, v63, v23
	v_mul_f32_e32 v40, v64, v24
	v_mul_f32_e32 v25, v65, v25
	v_fmac_f32_e32 v33, v22, v22
	v_fmac_f32_e32 v36, v24, v24
	v_mul_f32_e32 v38, v29, v29
	v_fmac_f32_e32 v37, v30, v30
	global_store_dwordx4 v[44:45], v[18:21], off
	v_fmac_f32_e32 v38, v28, v28
	v_mul_f32_e32 v41, v50, v30
	v_mul_f32_e32 v18, 0x41c00000, v39
	v_mul_f32_e32 v19, 0x41c00000, v23
	v_mul_f32_e32 v20, 0x41c00000, v40
	v_mul_f32_e32 v21, 0x41c00000, v25
	v_add_f32_e32 v25, v33, v36
	v_med3_f32 v18, v18, s51, v177
	v_med3_f32 v19, v19, s51, v177
	v_med3_f32 v20, v20, s51, v177
	v_med3_f32 v21, v21, s51, v177
	v_add_f32_e32 v25, v25, v37
	v_add_f32_e32 v18, 0x4b400000, v18
	v_add_f32_e32 v19, 0x4b400000, v19
	v_add_f32_e32 v20, 0x4b400000, v20
	v_add_f32_e32 v21, 0x4b400000, v21
	v_add_f32_e32 v25, v38, v25
	v_perm_b32 v18, v19, v18, s56
	v_perm_b32 v19, v21, v20, s57
	v_add_f32_e32 v21, v32, v25
	v_or_b32_e32 v20, v18, v19
	ds_bpermute_b32 v18, v132, v21
	v_mul_f32_e32 v19, v53, v29
	v_mul_f32_e32 v19, 0x41c00000, v19
	v_mul_f32_e32 v31, v51, v31
	v_mul_f32_e32 v42, v52, v28
	v_med3_f32 v19, v19, s51, v177
	s_waitcnt lgkmcnt(0)
	v_add_f32_e32 v18, v21, v18
	v_mul_f32_e32 v22, 0x41c00000, v41
	v_mul_f32_e32 v23, 0x41c00000, v31
	v_mul_f32_e32 v24, 0x41c00000, v42
	v_add_f32_e32 v25, 0x4b400000, v19
	ds_bpermute_b32 v19, v133, v18
	v_med3_f32 v22, v22, s51, v177
	v_med3_f32 v23, v23, s51, v177
	v_med3_f32 v24, v24, s51, v177
	v_add_f32_e32 v22, 0x4b400000, v22
	v_add_f32_e32 v23, 0x4b400000, v23
	v_add_f32_e32 v24, 0x4b400000, v24
	v_perm_b32 v21, v23, v22, s56
	v_perm_b32 v22, v25, v24, s57
	v_or_b32_e32 v21, v21, v22
	global_store_dwordx2 v[26:27], v[20:21], off offset:128
	s_and_saveexec_b64 s[28:29], s[0:1]
	s_cbranch_execz .LBB0_631
	v_lshlrev_b64 v[20:21], 8, v[34:35]
	v_lshl_add_u64 v[20:21], s[22:23], 0, v[20:21]
	s_waitcnt lgkmcnt(0)
	v_add_f32_e32 v18, v18, v19
	global_store_dword v[20:21], v18, off
; __device__ __forceinline__ unsigned cvt_pk_bf16(float lo, float hi) { unsigned r; asm volatile("v_cvt_pk_bf16_f32 %0, %1, %2" : "=v"(r) : "v"(lo), "v"(hi)); return r; }
;     __device__ __forceinline__ void operator()(const f32x4 (&acc)[2][2][4][2], const Unit& u, int wr, int wc, int fr, int fq) const {
;     ...
;             for (int m = 0; m < 4; ++m) { const size_t r = (size_t)(row0 + ai * HALF + m * 16); float ss = 0.f;
; #pragma unroll
;                 for (int bj = 0; bj < 2; ++bj) { const size_t off = r * 4096 + col0 + bj * HALF;
;                     const f32x4 v0 = acc[ai][bj][m][0] * scale + *(const f32x4*)(R + off), v1 = acc[ai][bj][m][1] * scale + *(const f32x4*)(R + off + 4);
;                     ss += (v0[0] * v0[0] + v0[1] * v0[1]) + (v0[2] * v0[2] + v0[3] * v0[3]) + (v1[0] * v1[0] + v1[1] * v1[1]) + (v1[2] * v1[2] + v1[3] * v1[3]);
;                     u32x4 w; w.x = cvt_pk_bf16(v0[0], v0[1]); w.y = cvt_pk_bf16(v0[2], v0[3]); w.z = cvt_pk_bf16(v1[0], v1[1]); w.w = cvt_pk_bf16(v1[2], v1[3]);
;                     *(u32x4*)(HB + off) = w;
;                     u32x2e q; q.x = q8x4(v0, gv[bj][0], (float)HQS); q.y = q8x4(v1, gv[bj][1], (float)HQS);
;                     *(u32x2e*)(Q8 + r * LDQ8 + col0 + bj * HALF) = q; }
;                 ss += __shfl_xor(ss, 16); ss += __shfl_xor(ss, 32);
;                 if (fq == 0) SSQP[r * 64 + u.pn * 4 + wc] = ss; }
.LBB0_631:
	s_or_b64 exec, exec, s[28:29]
	v_add_u32_e32 v18, 0xb0, v140
	s_waitcnt lgkmcnt(0)
	v_ashrrev_i32_e32 v19, 31, v18
	v_lshlrev_b64 v[20:21], 12, v[18:19]
	v_lshl_add_u64 v[28:29], v[20:21], 0, v[138:139]
	v_lshl_add_u64 v[30:31], v[28:29], 2, s[8:9]
	s_nop 0
	s_nop 0
	v_cvt_f32_i32_e32 v15, v15
	v_cvt_f32_i32_e32 v14, v14
	v_cvt_f32_i32_e32 v17, v17
	v_cvt_f32_i32_e32 v16, v16
	v_cvt_f32_i32_e32 v33, v11
	v_cvt_f32_i32_e32 v32, v10
	v_cvt_f32_i32_e32 v13, v13
	v_cvt_f32_i32_e32 v12, v12
	v_lshlrev_b64 v[28:29], 1, v[28:29]
	v_lshl_add_u64 v[34:35], s[14:15], 0, v[28:29]
	v_mad_i64_i32 v[10:11], s[28:29], v18, s50, v[142:143]
	v_cvt_f32_i32_e32 v7, v7
	v_cvt_f32_i32_e32 v6, v6
	v_cvt_f32_i32_e32 v9, v9
	v_cvt_f32_i32_e32 v8, v8
	v_cvt_f32_i32_e32 v3, v3
	v_cvt_f32_i32_e32 v2, v2
	v_cvt_f32_i32_e32 v5, v5
	v_cvt_f32_i32_e32 v4, v4
	v_or_b32_e32 v28, 0x100, v28
	v_lshl_add_u64 v[28:29], s[14:15], 0, v[28:29]
	s_waitcnt vmcnt(4)
	v_pk_fma_f32 v[16:17], v[16:17], s[26:27], v[214:215] op_sel_hi:[1,0,1]
	v_pk_fma_f32 v[36:37], v[14:15], s[26:27], v[212:213] op_sel_hi:[1,0,1]
	s_waitcnt vmcnt(4)
	v_pk_fma_f32 v[26:27], v[12:13], s[26:27], v[218:219] op_sel_hi:[1,0,1]
	v_pk_fma_f32 v[24:25], v[32:33], s[26:27], v[216:217] op_sel_hi:[1,0,1]
	v_cvt_pk_bf16_f32 v12, v36, v37
	v_cvt_pk_bf16_f32 v13, v16, v17
	v_mul_f32_e32 v20, v74, v36
	v_cvt_pk_bf16_f32 v14, v24, v25
	v_cvt_pk_bf16_f32 v15, v26, v27
	v_mul_f32_e32 v21, v75, v37
	v_mul_f32_e32 v22, v76, v16
	v_mul_f32_e32 v23, v77, v17
	v_mul_f32_e32 v32, v66, v24
	v_mul_f32_e32 v33, v67, v25
	v_mul_f32_e32 v38, v68, v26
	v_mul_f32_e32 v39, v69, v27
	global_store_dwordx4 v[34:35], v[12:15], off
	v_mul_f32_e32 v17, v17, v17
	v_fmac_f32_e32 v17, v16, v16
	v_mul_f32_e32 v12, 0x41c00000, v20
	v_mul_f32_e32 v13, 0x41c00000, v21
	v_mul_f32_e32 v14, 0x41c00000, v22
	v_mul_f32_e32 v15, 0x41c00000, v23
	v_mul_f32_e32 v20, 0x41c00000, v32
	v_mul_f32_e32 v21, 0x41c00000, v33
	v_mul_f32_e32 v22, 0x41c00000, v38
	v_mul_f32_e32 v23, 0x41c00000, v39
	v_med3_f32 v12, v12, s51, v177
	v_med3_f32 v13, v13, s51, v177
	v_med3_f32 v14, v14, s51, v177
	v_med3_f32 v15, v15, s51, v177
	v_med3_f32 v20, v20, s51, v177
	v_med3_f32 v21, v21, s51, v177
	v_med3_f32 v22, v22, s51, v177
	v_med3_f32 v23, v23, s51, v177
	v_add_f32_e32 v12, 0x4b400000, v12
	v_add_f32_e32 v13, 0x4b400000, v13
	v_add_f32_e32 v14, 0x4b400000, v14
	v_add_f32_e32 v15, 0x4b400000, v15
	v_add_f32_e32 v20, 0x4b400000, v20
	v_add_f32_e32 v21, 0x4b400000, v21
	v_add_f32_e32 v22, 0x4b400000, v22
	v_add_f32_e32 v23, 0x4b400000, v23
	v_perm_b32 v12, v13, v12, s56
	v_perm_b32 v13, v15, v14, s57
	v_perm_b32 v14, v21, v20, s56
	v_perm_b32 v15, v23, v22, s57
	v_or_b32_e32 v12, v12, v13
	v_or_b32_e32 v13, v14, v15
	global_store_dwordx2 v[10:11], v[12:13], off
	s_nop 0
	s_nop 0
	s_nop 0
	v_mul_f32_e32 v30, v37, v37
	v_fmac_f32_e32 v30, v36, v36
	v_mul_f32_e32 v25, v25, v25
	v_add_f32_e32 v16, v30, v17
	v_fmac_f32_e32 v25, v24, v24
	v_mul_f32_e32 v27, v27, v27
	v_fmac_f32_e32 v27, v26, v26
	v_add_f32_e32 v16, v16, v25
	v_add_f32_e32 v16, v27, v16
	s_waitcnt vmcnt(7)
	v_pk_fma_f32 v[8:9], v[8:9], s[26:27], v[222:223] op_sel_hi:[1,0,1]
	v_pk_fma_f32 v[6:7], v[6:7], s[26:27], v[220:221] op_sel_hi:[1,0,1]
	s_waitcnt vmcnt(7)
	v_pk_fma_f32 v[14:15], v[2:3], s[26:27], v[224:225] op_sel_hi:[1,0,1]
	v_mul_f32_e32 v17, v7, v7
	v_mul_f32_e32 v20, v9, v9
	v_pk_fma_f32 v[12:13], v[4:5], s[26:27], v[226:227] op_sel_hi:[1,0,1]
	v_mul_f32_e32 v21, v15, v15
	v_cvt_pk_bf16_f32 v2, v6, v7
	v_cvt_pk_bf16_f32 v3, v8, v9
	v_cvt_pk_bf16_f32 v4, v14, v15
	v_cvt_pk_bf16_f32 v5, v12, v13
	v_mul_f32_e32 v23, v62, v6
	v_mul_f32_e32 v7, v63, v7
	v_mul_f32_e32 v24, v64, v8
	v_mul_f32_e32 v9, v65, v9
	v_fmac_f32_e32 v17, v6, v6
	v_fmac_f32_e32 v20, v8, v8
	v_mul_f32_e32 v22, v13, v13
	v_fmac_f32_e32 v21, v14, v14
	global_store_dwordx4 v[28:29], v[2:5], off
	v_fmac_f32_e32 v22, v12, v12
	v_mul_f32_e32 v25, v50, v14
	v_mul_f32_e32 v2, 0x41c00000, v23
	v_mul_f32_e32 v3, 0x41c00000, v7
	v_mul_f32_e32 v4, 0x41c00000, v24
	v_mul_f32_e32 v5, 0x41c00000, v9
	v_add_f32_e32 v9, v17, v20
	v_med3_f32 v2, v2, s51, v177
	v_med3_f32 v3, v3, s51, v177
	v_med3_f32 v4, v4, s51, v177
	v_med3_f32 v5, v5, s51, v177
	v_add_f32_e32 v9, v9, v21
	v_add_f32_e32 v2, 0x4b400000, v2
	v_add_f32_e32 v3, 0x4b400000, v3
	v_add_f32_e32 v4, 0x4b400000, v4
	v_add_f32_e32 v5, 0x4b400000, v5
	v_add_f32_e32 v9, v22, v9
	v_perm_b32 v2, v3, v2, s56
	v_perm_b32 v3, v5, v4, s57
	v_add_f32_e32 v5, v16, v9
	v_or_b32_e32 v4, v2, v3
	ds_bpermute_b32 v2, v132, v5
	v_mul_f32_e32 v3, v53, v13
	v_mul_f32_e32 v3, 0x41c00000, v3
	v_mul_f32_e32 v15, v51, v15
	v_mul_f32_e32 v26, v52, v12
	v_med3_f32 v3, v3, s51, v177
	s_waitcnt lgkmcnt(0)
	v_add_f32_e32 v2, v5, v2
	v_mul_f32_e32 v6, 0x41c00000, v25
	v_mul_f32_e32 v7, 0x41c00000, v15
	v_mul_f32_e32 v8, 0x41c00000, v26
	v_add_f32_e32 v9, 0x4b400000, v3
	ds_bpermute_b32 v3, v133, v2
	v_med3_f32 v6, v6, s51, v177
	v_med3_f32 v7, v7, s51, v177
	v_med3_f32 v8, v8, s51, v177
	v_add_f32_e32 v6, 0x4b400000, v6
	v_add_f32_e32 v7, 0x4b400000, v7
	v_add_f32_e32 v8, 0x4b400000, v8
	v_perm_b32 v5, v7, v6, s56
	v_perm_b32 v6, v9, v8, s57
	v_or_b32_e32 v5, v5, v6
	global_store_dwordx2 v[10:11], v[4:5], off offset:128
	s_and_saveexec_b64 s[28:29], s[0:1]
	s_cbranch_execz .LBB0_633
	v_lshlrev_b64 v[4:5], 8, v[18:19]
	v_lshl_add_u64 v[4:5], s[22:23], 0, v[4:5]
	s_waitcnt lgkmcnt(0)
	v_add_f32_e32 v2, v2, v3
	global_store_dword v[4:5], v2, off

; #define LAS __attribute__((address_space(3)))
; __global__ void __launch_bounds__(NWAVES * 64, 2) fwd(Args args) {
;     extern __shared__ __attribute__((aligned(16))) unsigned char lds[];
;     Frame F;
;     F.lds = (LAS unsigned char*)lds;
;     F.MISC = (volatile LAS unsigned*)(F.lds + MISC_OFF);
;     F.tid = threadIdx.x; F.lane = F.tid & 63; F.wave = __builtin_amdgcn_readfirstlane(F.tid >> 6);
	.amdhsa_kernel _Z3fwd4Args
		.amdhsa_group_segment_fixed_size 0
		.amdhsa_private_segment_fixed_size 0
		.amdhsa_kernarg_size 392
		.amdhsa_user_sgpr_count 2
		.amdhsa_user_sgpr_dispatch_ptr 0
		.amdhsa_user_sgpr_queue_ptr 0
		.amdhsa_user_sgpr_kernarg_segment_ptr 1
		.amdhsa_user_sgpr_dispatch_id 0
		.amdhsa_user_sgpr_kernarg_preload_length 0
		.amdhsa_user_sgpr_kernarg_preload_offset 0
		.amdhsa_user_sgpr_private_segment_size 0
		.amdhsa_uses_dynamic_stack 0
		.amdhsa_enable_private_segment 0
		.amdhsa_system_sgpr_workgroup_id_x 1
		.amdhsa_system_sgpr_workgroup_id_y 0
		.amdhsa_system_sgpr_workgroup_id_z 0
		.amdhsa_system_sgpr_workgroup_info 0
		.amdhsa_system_vgpr_workitem_id 0
		.amdhsa_next_free_vgpr 256
		.amdhsa_next_free_sgpr 102
		.amdhsa_accum_offset 256
		.amdhsa_reserve_vcc 1
		.amdhsa_float_round_mode_32 0
		.amdhsa_float_round_mode_16_64 0
		.amdhsa_float_denorm_mode_32 3
		.amdhsa_float_denorm_mode_16_64 3
		.amdhsa_dx10_clamp 1
		.amdhsa_ieee_mode 1
		.amdhsa_fp16_overflow 0
		.amdhsa_tg_split 0
		.amdhsa_exception_fp_ieee_invalid_op 0
		.amdhsa_exception_fp_denorm_src 0
		.amdhsa_exception_fp_ieee_div_zero 0
		.amdhsa_exception_fp_ieee_overflow 0
		.amdhsa_exception_fp_ieee_underflow 0
		.amdhsa_exception_fp_ieee_inexact 0
		.amdhsa_exception_int_div_zero 0
	.end_amdhsa_kernel

; #define LAS __attribute__((address_space(3)))
; __global__ void __launch_bounds__(NWAVES * 64, 2) fwd(Args args) {
;     extern __shared__ __attribute__((aligned(16))) unsigned char lds[];
;     Frame F;
;     F.lds = (LAS unsigned char*)lds;
;     F.MISC = (volatile LAS unsigned*)(F.lds + MISC_OFF);
;     F.tid = threadIdx.x; F.lane = F.tid & 63; F.wave = __builtin_amdgcn_readfirstlane(F.tid >> 6);
amdhsa.kernels:
  - .agpr_count:     0
    .args:
      - .offset:         0
        .size:           136
        .value_kind:     by_value
      - .offset:         136
        .size:           4
        .value_kind:     hidden_block_count_x
      - .offset:         140
        .size:           4
        .value_kind:     hidden_block_count_y
      - .offset:         144
        .size:           4
        .value_kind:     hidden_block_count_z
      - .offset:         148
        .size:           2
        .value_kind:     hidden_group_size_x
      - .offset:         150
        .size:           2
        .value_kind:     hidden_group_size_y
      - .offset:         152
        .size:           2
        .value_kind:     hidden_group_size_z
      - .offset:         154
        .size:           2
        .value_kind:     hidden_remainder_x
      - .offset:         156
        .size:           2
        .value_kind:     hidden_remainder_y
      - .offset:         158
        .size:           2
        .value_kind:     hidden_remainder_z
      - .offset:         176
        .size:           8
        .value_kind:     hidden_global_offset_x
      - .offset:         184
        .size:           8
        .value_kind:     hidden_global_offset_y
      - .offset:         192
        .size:           8
        .value_kind:     hidden_global_offset_z
      - .offset:         200
        .size:           2
        .value_kind:     hidden_grid_dims
      - .offset:         256
        .size:           4
        .value_kind:     hidden_dynamic_lds_size
    .group_segment_fixed_size: 0
    .kernarg_segment_align: 8
    .kernarg_segment_size: 392
    .language:       OpenCL C
    .language_version:
      - 2
      - 0
    .max_flat_workgroup_size: 512
    .name:           _Z3fwd4Args
    .private_segment_fixed_size: 0
    .sgpr_count:     108
    .sgpr_spill_count: 61
    .symbol:         _Z3fwd4Args.kd
    .uniform_work_group_size: 1
    .uses_dynamic_stack: false
    .vgpr_count:     256
    .vgpr_spill_count: 0
    .wavefront_size: 64
